# P6 norm2/modulate: gain/scale/shift loads hoisted into free VGPR quads (all in flight), counted vmcnt
# speedup vs baseline: 1.0080x; 1.0028x over previous
.LBB0_2123:
	v_lshl_add_u64 v[28:29], s[44:45], 0, v[16:17]
	v_add_co_u32_e32 v4, vcc, 0x37a00000, v28
	s_add_i32 s0, s80, s8
	s_nop 0
	v_addc_co_u32_e32 v5, vcc, 0, v29, vcc
	global_load_dwordx2 v[62:63], v[4:5], off
	global_load_dwordx2 v[60:61], v[4:5], off offset:512
	global_load_dwordx2 v[48:49], v[4:5], off offset:1024
	s_waitcnt lgkmcnt(0)
	global_load_dwordx2 v[6:7], v[4:5], off offset:1536
	global_load_dwordx2 v[46:47], v[4:5], off offset:2048
	global_load_dwordx2 v[44:45], v[4:5], off offset:2560
	global_load_dwordx2 v[42:43], v[4:5], off offset:3072
	s_nop 0
	global_load_dwordx2 v[4:5], v[4:5], off offset:3584
	s_cmp_lt_i32 s0, s86
	s_cselect_b32 s48, s0, s8
	s_ashr_i32 s49, s48, 31
	s_lshl_b64 s[50:51], s[48:49], 12
	v_mov_b32_e32 v2, s81
	s_min_i32 s0, s8, 0x4000
	s_lshr_b32 s0, s0, 12
	s_mulk_i32 s0, 0x3000
	s_ashr_i32 s1, s0, 31
	s_lshl_b64 s[0:1], s[0:1], 2
	s_add_u32 s2, s6, s0
	s_addc_u32 s3, s7, s1
	s_min_i32 s0, s48, 0x4000
	s_lshr_b32 s0, s0, 12
	s_mulk_i32 s0, 0x3000
	s_ashr_i32 s1, s0, 31
	s_lshl_b64 s[0:1], s[0:1], 2
	s_add_u32 s0, s6, s0
	s_addc_u32 s1, s7, s1
	s_waitcnt vmcnt(7)
	v_and_b32_e32 v103, 0xffff0000, v63
	v_and_b32_e32 v101, 0xffff0000, v62
	v_lshlrev_b32_e32 v102, 16, v63
	s_waitcnt vmcnt(4)
	v_lshlrev_b32_e32 v25, 16, v6
	s_waitcnt vmcnt(0)
	v_lshlrev_b32_e32 v21, 16, v4
	v_and_b32_e32 v19, 0xffff0000, v4
	v_lshlrev_b32_e32 v58, 16, v5
	v_and_b32_e32 v59, 0xffff0000, v5
	v_lshl_add_u64 v[4:5], v[8:9], 0, s[50:51]
	v_and_b32_e32 v23, 0xffff0000, v6
	v_lshlrev_b32_e32 v26, 16, v7
	v_and_b32_e32 v27, 0xffff0000, v7
	global_load_dwordx2 v[40:41], v[4:5], off
	global_load_dwordx2 v[38:39], v[4:5], off offset:512
	global_load_dwordx2 v[36:37], v[4:5], off offset:1024
	global_load_dwordx2 v[6:7], v[4:5], off offset:1536
	global_load_dwordx2 v[34:35], v[4:5], off offset:2048
	global_load_dwordx2 v[32:33], v[4:5], off offset:2560
	global_load_dwordx2 v[30:31], v[4:5], off offset:3072
	global_load_dwordx2 v[50:51], v[4:5], off offset:3584
	ds_read_b64 v[64:65], v2
	v_mul_f32_e32 v2, v103, v103
	v_lshlrev_b32_e32 v100, 16, v62
	v_pk_fma_f32 v[62:63], v[102:103], v[102:103], v[2:3] op_sel_hi:[1,1,0]
	v_and_b32_e32 v99, 0xffff0000, v61
	v_and_b32_e32 v98, 0xffff0000, v60
	v_mul_f32_e32 v2, v101, v101
	v_lshlrev_b32_e32 v95, 16, v61
	v_lshlrev_b32_e32 v94, 16, v60
	v_pk_mul_f32 v[60:61], v[98:99], v[98:99]
	v_lshlrev_b32_e32 v90, 16, v48
	v_and_b32_e32 v91, 0xffff0000, v48
	v_lshlrev_b32_e32 v96, 16, v49
	v_and_b32_e32 v97, 0xffff0000, v49
	v_pk_fma_f32 v[48:49], v[100:101], v[100:101], v[2:3] op_sel_hi:[1,1,0]
	s_waitcnt lgkmcnt(0)
	v_readfirstlane_b32 s9, v64
	v_readfirstlane_b32 s12, v65
	v_pk_fma_f32 v[60:61], v[94:95], v[94:95], v[60:61]
	v_mov_b32_e32 v24, v48
	v_mov_b32_e32 v64, v62
	v_mov_b32_e32 v65, v25
	v_mul_f32_e32 v4, v23, v23
	v_pk_add_f32 v[48:49], v[48:49], v[62:63]
	v_pk_mul_f32 v[62:63], v[24:25], v[64:65]
	v_pk_add_f32 v[60:61], v[60:61], v[60:61] op_sel:[0,1] op_sel_hi:[1,0]
	v_mov_b32_e32 v49, v63
	v_mov_b32_e32 v61, v4
	v_mul_f32_e32 v2, v91, v91
	v_pk_add_f32 v[48:49], v[48:49], v[60:61]
	v_pk_fma_f32 v[60:61], v[90:91], v[90:91], v[2:3] op_sel_hi:[1,1,0]
	v_mul_f32_e32 v2, v97, v97
	v_mul_f32_e32 v18, v27, v27
	v_pk_fma_f32 v[62:63], v[96:97], v[96:97], v[2:3] op_sel_hi:[1,1,0]
	v_and_b32_e32 v107, 0xffff0000, v47
	v_mov_b32_e32 v63, v18
	v_and_b32_e32 v106, 0xffff0000, v46
	v_lshlrev_b32_e32 v105, 16, v47
	v_lshlrev_b32_e32 v104, 16, v46
	v_pk_mul_f32 v[46:47], v[106:107], v[106:107]
	v_and_b32_e32 v93, 0xffff0000, v45
	v_pk_fma_f32 v[46:47], v[104:105], v[104:105], v[46:47]
	v_and_b32_e32 v92, 0xffff0000, v44
	v_pk_add_f32 v[46:47], v[46:47], v[46:47] op_sel:[0,1] op_sel_hi:[1,0]
	v_lshlrev_b32_e32 v89, 16, v45
	v_lshlrev_b32_e32 v88, 16, v44
	v_pk_mul_f32 v[44:45], v[92:93], v[92:93]
	v_lshlrev_b32_e32 v78, 16, v42
	v_and_b32_e32 v79, 0xffff0000, v42
	v_lshlrev_b32_e32 v80, 16, v43
	v_and_b32_e32 v81, 0xffff0000, v43
	v_pk_fma_f32 v[44:45], v[88:89], v[88:89], v[44:45]
	v_mul_f32_e32 v2, v19, v19
	v_pk_add_f32 v[44:45], v[44:45], v[44:45] op_sel:[0,1] op_sel_hi:[1,0]
	s_add_u32 s52, s9, s46
	v_mov_b32_e32 v45, v2
	v_mul_f32_e32 v2, v79, v79
	s_addc_u32 s53, s12, s47
	s_add_u32 s58, s2, 0x6000
	v_mul_f32_e32 v4, v58, v58
	s_addc_u32 s59, s3, 0
	s_add_u32 s60, s2, 0x8000
	s_addc_u32 s61, s3, 0
	s_add_u32 s54, s0, 0x6000
	s_addc_u32 s55, s1, 0
	s_add_u32 s56, s0, 0x8000
	s_mov_b32 s0, 0x3a000000
	s_addc_u32 s57, s1, 0
	v_mov_b32_e32 v22, v25
	s_waitcnt vmcnt(7)
	v_and_b32_e32 v73, 0xffff0000, v41
	v_and_b32_e32 v71, 0xffff0000, v40
	v_lshlrev_b32_e32 v72, 16, v41
	s_waitcnt vmcnt(4)
	v_lshlrev_b32_e32 v55, 16, v6
	v_and_b32_e32 v53, 0xffff0000, v6
	v_mul_f32_e32 v6, v26, v26
	v_mov_b32_e32 v61, v6
	v_pk_add_f32 v[60:61], v[60:61], v[62:63]
	v_mul_f32_e32 v6, v59, v59
	v_pk_add_f32 v[48:49], v[48:49], v[60:61]
	v_lshlrev_b32_e32 v70, 16, v40
	v_pk_add_f32 v[42:43], v[48:49], v[48:49] op_sel:[0,1] op_sel_hi:[1,0]
	v_mov_b32_e32 v48, v46
	v_mov_b32_e32 v20, v42
	v_mov_b32_e32 v49, v21
	v_pk_add_f32 v[42:43], v[42:43], v[46:47]
	v_pk_mul_f32 v[46:47], v[20:21], v[48:49]
	v_and_b32_e32 v77, 0xffff0000, v39
	v_mov_b32_e32 v43, v47
	v_pk_add_f32 v[42:43], v[42:43], v[44:45]
	v_pk_fma_f32 v[44:45], v[78:79], v[78:79], v[2:3] op_sel_hi:[1,1,0]
	v_mul_f32_e32 v2, v81, v81
	v_pk_fma_f32 v[46:47], v[80:81], v[80:81], v[2:3] op_sel_hi:[1,1,0]
	v_mov_b32_e32 v45, v4
	v_mov_b32_e32 v47, v6
	v_pk_add_f32 v[44:45], v[44:45], v[46:47]
	v_mul_f32_e32 v2, v73, v73
	v_pk_add_f32 v[108:109], v[42:43], v[44:45]
	global_load_dwordx4 v[118:121], v181, s[52:53]
	global_load_dwordx4 v[122:125], v181, s[60:61]
	global_load_dwordx4 v[126:129], v181, s[58:59]
	global_load_dwordx4 v[130:133], v181, s[52:53] offset:1024
	global_load_dwordx4 v[134:137], v182, s[60:61]
	global_load_dwordx4 v[138:141], v182, s[58:59]
	global_load_dwordx4 v[142:145], v181, s[52:53] offset:2048
	global_load_dwordx4 v[146:149], v183, s[60:61]
	global_load_dwordx4 v[150:153], v183, s[58:59]
	global_load_dwordx4 v[154:157], v181, s[52:53] offset:3072
	global_load_dwordx4 v[158:161], v184, s[60:61]
	global_load_dwordx4 v[162:165], v184, s[58:59]
	global_load_dwordx4 v[166:169], v185, s[52:53]
	global_load_dwordx4 v[170:173], v185, s[60:61]
	global_load_dwordx4 v[174:177], v185, s[58:59]
	global_load_dwordx4 v[214:217], v186, s[52:53]
	global_load_dwordx4 v[224:227], v186, s[60:61]
	global_load_dwordx4 v[228:231], v186, s[58:59]
	global_load_dwordx4 v[232:235], v187, s[52:53]
	global_load_dwordx4 v[236:239], v187, s[60:61]
	global_load_dwordx4 v[240:243], v187, s[58:59]
	global_load_dwordx4 v[244:247], v190, s[52:53]
	global_load_dwordx4 v[248:251], v190, s[60:61]
	v_pk_fma_f32 v[40:41], v[72:73], v[72:73], v[2:3] op_sel_hi:[1,1,0]
	v_and_b32_e32 v76, 0xffff0000, v38
	v_mul_f32_e32 v2, v71, v71
	v_lshlrev_b32_e32 v75, 16, v39
	v_lshlrev_b32_e32 v74, 16, v38
	v_pk_mul_f32 v[38:39], v[76:77], v[76:77]
	v_lshlrev_b32_e32 v62, 16, v36
	v_and_b32_e32 v63, 0xffff0000, v36
	v_lshlrev_b32_e32 v64, 16, v37
	v_and_b32_e32 v65, 0xffff0000, v37
	v_pk_fma_f32 v[36:37], v[70:71], v[70:71], v[2:3] op_sel_hi:[1,1,0]
	v_pk_fma_f32 v[38:39], v[74:75], v[74:75], v[38:39]
	v_mov_b32_e32 v54, v36
	v_mul_f32_e32 v4, v53, v53
	v_pk_add_f32 v[36:37], v[36:37], v[40:41]
	v_pk_add_f32 v[38:39], v[38:39], v[38:39] op_sel:[0,1] op_sel_hi:[1,0]
	v_mul_f32_e32 v2, v63, v63
	v_mov_b32_e32 v39, v4
	v_lshlrev_b32_e32 v56, 16, v7
	v_and_b32_e32 v57, 0xffff0000, v7
	v_mul_f32_e32 v6, v56, v56
	v_mul_f32_e32 v18, v57, v57
	s_waitcnt vmcnt(26)
	v_and_b32_e32 v69, 0xffff0000, v35
	v_and_b32_e32 v68, 0xffff0000, v34
	v_lshlrev_b32_e32 v67, 16, v35
	v_lshlrev_b32_e32 v66, 16, v34
	v_pk_mul_f32 v[34:35], v[68:69], v[68:69]
	s_waitcnt vmcnt(25)
	v_and_b32_e32 v87, 0xffff0000, v33
	v_pk_fma_f32 v[34:35], v[66:67], v[66:67], v[34:35]
	v_and_b32_e32 v86, 0xffff0000, v32
	s_waitcnt vmcnt(23)
	v_lshlrev_b32_e32 v7, 16, v50
	v_pk_add_f32 v[34:35], v[34:35], v[34:35] op_sel:[0,1] op_sel_hi:[1,0]
	v_lshlrev_b32_e32 v61, 16, v33
	v_lshlrev_b32_e32 v60, 16, v32
	v_pk_mul_f32 v[32:33], v[86:87], v[86:87]
	v_lshlrev_b32_e32 v82, 16, v30
	v_and_b32_e32 v83, 0xffff0000, v30
	v_lshlrev_b32_e32 v84, 16, v31
	v_and_b32_e32 v85, 0xffff0000, v31
	v_and_b32_e32 v5, 0xffff0000, v50
	v_pk_fma_f32 v[32:33], v[60:61], v[60:61], v[32:33]
	v_lshlrev_b32_e32 v50, 16, v51
	v_pk_add_f32 v[32:33], v[32:33], v[32:33] op_sel:[0,1] op_sel_hi:[1,0]
	v_and_b32_e32 v51, 0xffff0000, v51
	v_mul_f32_e32 v4, v50, v50
	v_mov_b32_e32 v52, v55
	s_waitcnt vmcnt(21)
	v_mov_b32_e32 v42, v118
	v_mov_b32_e32 v43, v119
	v_mov_b32_e32 v44, v120
	v_mov_b32_e32 v45, v121
	v_mov_b32_e32 v46, v122
	v_mov_b32_e32 v47, v123
	v_mov_b32_e32 v48, v124
	v_mov_b32_e32 v49, v125
	global_load_dwordx4 v[118:121], v190, s[58:59]
	global_load_dwordx4 v[122:125], v181, s[52:53]
	v_pk_add_f32 v[212:213], v[46:47], 1.0 op_sel_hi:[1,0]
	v_mov_b32_e32 v46, v40
	v_mov_b32_e32 v47, v55
	v_pk_mul_f32 v[40:41], v[54:55], v[46:47]
	v_pk_add_f32 v[48:49], v[48:49], 1.0 op_sel_hi:[1,0]
	v_mov_b32_e32 v37, v41
	v_pk_add_f32 v[36:37], v[36:37], v[38:39]
	v_pk_fma_f32 v[38:39], v[62:63], v[62:63], v[2:3] op_sel_hi:[1,1,0]
	v_mul_f32_e32 v2, v65, v65
	v_pk_fma_f32 v[40:41], v[64:65], v[64:65], v[2:3] op_sel_hi:[1,1,0]
	v_mov_b32_e32 v39, v6
	v_mov_b32_e32 v41, v18
	v_pk_add_f32 v[38:39], v[38:39], v[40:41]
	v_mul_f32_e32 v2, v5, v5
	v_pk_add_f32 v[36:37], v[36:37], v[38:39]
	v_mov_b32_e32 v33, v2
	v_pk_add_f32 v[30:31], v[36:37], v[36:37] op_sel:[0,1] op_sel_hi:[1,0]
	v_mov_b32_e32 v36, v34
	v_mov_b32_e32 v6, v30
	v_mov_b32_e32 v37, v7
	v_pk_add_f32 v[30:31], v[30:31], v[34:35]
	v_pk_mul_f32 v[34:35], v[6:7], v[36:37]
	v_mul_f32_e32 v2, v83, v83
	v_mov_b32_e32 v31, v35
	v_pk_add_f32 v[30:31], v[30:31], v[32:33]
	v_pk_fma_f32 v[32:33], v[82:83], v[82:83], v[2:3] op_sel_hi:[1,1,0]
	v_mul_f32_e32 v2, v85, v85
	v_mul_f32_e32 v18, v51, v51
	v_pk_fma_f32 v[34:35], v[84:85], v[84:85], v[2:3] op_sel_hi:[1,1,0]
	v_mov_b32_e32 v33, v4
	v_mov_b32_e32 v35, v18
	v_pk_add_f32 v[32:33], v[32:33], v[34:35]
	v_mov_b32_e32 v40, v95
	v_pk_add_f32 v[30:31], v[30:31], v[32:33]
	v_mov_b32_e32 v33, v108
	v_mov_b32_e32 v32, v30
	v_mov_b32_e32 v108, v31
	v_pk_add_f32 v[30:31], v[32:33], v[108:109]
	v_mov_b32_e32 v41, v99
	v_mov_b32_e32 v95, v98
	v_mov_b32_dpp v33, v31 quad_perm:[1,0,3,2] row_mask:0xf bank_mask:0xf bound_ctrl:1
	v_mov_b32_dpp v32, v30 quad_perm:[1,0,3,2] row_mask:0xf bank_mask:0xf bound_ctrl:1
	v_pk_add_f32 v[30:31], v[30:31], v[32:33]
	v_mov_b32_e32 v18, v21
	s_nop 0
	v_mov_b32_dpp v33, v31 quad_perm:[2,3,0,1] row_mask:0xf bank_mask:0xf bound_ctrl:1
	v_mov_b32_dpp v32, v30 quad_perm:[2,3,0,1] row_mask:0xf bank_mask:0xf bound_ctrl:1
	v_pk_add_f32 v[30:31], v[30:31], v[32:33]
	s_nop 1
	v_mov_b32_dpp v33, v31 row_half_mirror row_mask:0xf bank_mask:0xf bound_ctrl:1
	v_mov_b32_dpp v32, v30 row_half_mirror row_mask:0xf bank_mask:0xf bound_ctrl:1
	v_pk_add_f32 v[30:31], v[30:31], v[32:33]
	s_nop 1
	v_mov_b32_dpp v33, v31 row_mirror row_mask:0xf bank_mask:0xf bound_ctrl:1
	v_mov_b32_dpp v32, v30 row_mirror row_mask:0xf bank_mask:0xf bound_ctrl:1
	v_pk_add_f32 v[30:31], v[30:31], v[32:33]
	ds_bpermute_b32 v33, v111, v31
	ds_bpermute_b32 v32, v111, v30
	s_waitcnt lgkmcnt(0)
	v_pk_add_f32 v[30:31], v[30:31], v[32:33]
	ds_bpermute_b32 v33, v112, v31
	ds_bpermute_b32 v32, v112, v30
	s_waitcnt lgkmcnt(0)
	v_pk_add_f32 v[30:31], v[30:31], v[32:33]
	s_nop 0
	v_pk_fma_f32 v[108:109], v[30:31], s[0:1], v[188:189] op_sel_hi:[1,0,0]
	s_nop 0
	v_mul_f32_e32 v2, 0x4b800000, v109
	v_cmp_gt_f32_e64 s[0:1], s11, v109
	v_cmp_gt_f32_e32 vcc, s11, v108
	s_nop 0
	v_cndmask_b32_e64 v2, v109, v2, s[0:1]
	v_rsq_f32_e32 v2, v2
	s_nop 0
	v_mul_f32_e32 v4, 0x45800000, v2
	v_cndmask_b32_e64 v2, v2, v4, s[0:1]
	v_pk_mul_f32 v[30:31], v[2:3], v[102:103] op_sel_hi:[0,1]
	v_pk_mul_f32 v[32:33], v[2:3], v[100:101] op_sel_hi:[0,1]
	v_pk_mul_f32 v[32:33], v[42:43], v[32:33]
	v_pk_mul_f32 v[30:31], v[44:45], v[30:31]
	s_mov_b32 s0, 0x40200000
	s_waitcnt vmcnt(22)
	v_mov_b32_e32 v192, v126
	v_mov_b32_e32 v193, v127
	v_mov_b32_e32 v194, v128
	v_mov_b32_e32 v195, v129
	global_load_dwordx4 v[126:129], v181, s[56:57]
	v_pk_fma_f32 v[46:47], v[48:49], v[30:31], v[194:195]
	v_pk_fma_f32 v[48:49], v[212:213], v[32:33], v[192:193]
	v_add_co_u32_e64 v100, s[0:1], s0, v28
	v_cvt_pk_bf16_f32 v30, v48, v49
	v_cvt_pk_bf16_f32 v31, v46, v47
	v_addc_co_u32_e64 v101, s[0:1], 0, v29, s[0:1]
	global_store_dwordx2 v[100:101], v[30:31], off
	s_nop 0
	v_pk_mul_f32 v[40:41], v[2:3], v[40:41] op_sel_hi:[0,1]
	v_pk_mul_f32 v[42:43], v[2:3], v[94:95] op_sel_hi:[0,1]
	v_pk_mul_f32 v[90:91], v[2:3], v[90:91] op_sel_hi:[0,1]
	v_pk_mul_f32 v[26:27], v[2:3], v[26:27] op_sel_hi:[0,1]
	v_pk_mul_f32 v[22:23], v[2:3], v[22:23] op_sel_hi:[0,1]
	v_pk_mul_f32 v[80:81], v[2:3], v[80:81] op_sel_hi:[0,1]
	v_pk_mul_f32 v[78:79], v[2:3], v[78:79] op_sel_hi:[0,1]
	v_pk_mul_f32 v[58:59], v[2:3], v[58:59] op_sel_hi:[0,1]
	v_pk_mul_f32 v[18:19], v[2:3], v[18:19] op_sel_hi:[0,1]
	s_waitcnt vmcnt(23)
	v_mov_b32_e32 v28, v130
	v_mov_b32_e32 v29, v131
	v_mov_b32_e32 v30, v132
	v_mov_b32_e32 v31, v133
	global_load_dwordx4 v[130:133], v181, s[54:55]
	v_pk_mul_f32 v[28:29], v[28:29], v[42:43]
	v_pk_mul_f32 v[30:31], v[30:31], v[40:41]
	s_waitcnt vmcnt(23)
	v_mov_b32_e32 v32, v134
	v_mov_b32_e32 v33, v135
	v_mov_b32_e32 v34, v136
	v_mov_b32_e32 v35, v137
	global_load_dwordx4 v[134:137], v181, s[52:53] offset:1024
	v_pk_add_f32 v[34:35], v[34:35], 1.0 op_sel_hi:[1,0]
	v_pk_add_f32 v[32:33], v[32:33], 1.0 op_sel_hi:[1,0]
	s_waitcnt vmcnt(23)
	v_mov_b32_e32 v36, v138
	v_mov_b32_e32 v37, v139
	v_mov_b32_e32 v38, v140
	v_mov_b32_e32 v39, v141
	global_load_dwordx4 v[138:141], v182, s[56:57]
	v_pk_fma_f32 v[42:43], v[34:35], v[30:31], v[38:39]
	v_pk_fma_f32 v[44:45], v[32:33], v[28:29], v[36:37]
	v_cvt_pk_bf16_f32 v29, v42, v43
	v_cvt_pk_bf16_f32 v28, v44, v45
	global_store_dwordx2 v[100:101], v[28:29], off offset:512
	s_nop 0
	v_pk_mul_f32 v[40:41], v[2:3], v[96:97] op_sel_hi:[0,1]
	s_waitcnt vmcnt(24)
	v_mov_b32_e32 v28, v142
	v_mov_b32_e32 v29, v143
	v_mov_b32_e32 v30, v144
	v_mov_b32_e32 v31, v145
	global_load_dwordx4 v[142:145], v182, s[54:55]
	v_pk_mul_f32 v[28:29], v[28:29], v[90:91]
	v_pk_mul_f32 v[30:31], v[30:31], v[40:41]
	s_waitcnt vmcnt(24)
	v_mov_b32_e32 v32, v146
	v_mov_b32_e32 v33, v147
	v_mov_b32_e32 v34, v148
	v_mov_b32_e32 v35, v149
	global_load_dwordx4 v[146:149], v181, s[52:53] offset:2048
	v_pk_add_f32 v[34:35], v[34:35], 1.0 op_sel_hi:[1,0]
	v_pk_add_f32 v[32:33], v[32:33], 1.0 op_sel_hi:[1,0]
	s_waitcnt vmcnt(24)
	v_mov_b32_e32 v36, v150
	v_mov_b32_e32 v37, v151
	v_mov_b32_e32 v38, v152
	v_mov_b32_e32 v39, v153
	global_load_dwordx4 v[150:153], v183, s[56:57]
	v_pk_fma_f32 v[38:39], v[34:35], v[30:31], v[38:39]
	v_pk_fma_f32 v[40:41], v[32:33], v[28:29], v[36:37]
	v_cvt_pk_bf16_f32 v29, v38, v39
	v_cvt_pk_bf16_f32 v28, v40, v41
	global_store_dwordx2 v[100:101], v[28:29], off offset:1024
	s_nop 0
	v_mov_b32_e32 v90, v89
	v_mov_b32_e32 v91, v93
	v_mov_b32_e32 v89, v92
	v_pk_mul_f32 v[90:91], v[2:3], v[90:91] op_sel_hi:[0,1]
	v_pk_mul_f32 v[88:89], v[2:3], v[88:89] op_sel_hi:[0,1]
	s_waitcnt vmcnt(25)
	v_mov_b32_e32 v28, v154
	v_mov_b32_e32 v29, v155
	v_mov_b32_e32 v30, v156
	v_mov_b32_e32 v31, v157
	global_load_dwordx4 v[154:157], v183, s[54:55]
	v_pk_mul_f32 v[22:23], v[22:23], v[28:29]
	v_pk_mul_f32 v[24:25], v[26:27], v[30:31]
	s_waitcnt vmcnt(25)
	v_mov_b32_e32 v32, v158
	v_mov_b32_e32 v33, v159
	v_mov_b32_e32 v34, v160
	v_mov_b32_e32 v35, v161
	global_load_dwordx4 v[158:161], v181, s[52:53] offset:3072
	v_pk_add_f32 v[26:27], v[34:35], 1.0 op_sel_hi:[1,0]
	v_pk_add_f32 v[28:29], v[32:33], 1.0 op_sel_hi:[1,0]
	s_waitcnt vmcnt(25)
	v_mov_b32_e32 v94, v162
	v_mov_b32_e32 v95, v163
	v_mov_b32_e32 v96, v164
	v_mov_b32_e32 v97, v165
	global_load_dwordx4 v[162:165], v184, s[56:57]
	v_pk_fma_f32 v[30:31], v[24:25], v[26:27], v[96:97]
	v_pk_fma_f32 v[32:33], v[22:23], v[28:29], v[94:95]
	v_cvt_pk_bf16_f32 v23, v30, v31
	v_cvt_pk_bf16_f32 v22, v32, v33
	global_store_dwordx2 v[100:101], v[22:23], off offset:1536
	s_nop 0
	v_mov_b32_e32 v34, v105
	v_mov_b32_e32 v35, v107
	v_mov_b32_e32 v105, v106
	v_pk_mul_f32 v[34:35], v[2:3], v[34:35] op_sel_hi:[0,1]
	v_pk_mul_f32 v[36:37], v[2:3], v[104:105] op_sel_hi:[0,1]
	v_mul_f32_e32 v2, 0x4b800000, v108
	v_cndmask_b32_e32 v2, v108, v2, vcc
	v_rsq_f32_e32 v2, v2
	s_waitcnt vmcnt(26)
	v_mov_b32_e32 v22, v166
	v_mov_b32_e32 v23, v167
	v_mov_b32_e32 v24, v168
	v_mov_b32_e32 v25, v169
	global_load_dwordx4 v[166:169], v184, s[54:55]
	v_pk_mul_f32 v[22:23], v[36:37], v[22:23]
	v_pk_mul_f32 v[24:25], v[34:35], v[24:25]
	s_waitcnt vmcnt(26)
	v_mov_b32_e32 v26, v170
	v_mov_b32_e32 v27, v171
	v_mov_b32_e32 v28, v172
	v_mov_b32_e32 v29, v173
	global_load_dwordx4 v[170:173], v185, s[52:53]
	v_pk_add_f32 v[28:29], v[28:29], 1.0 op_sel_hi:[1,0]
	v_pk_add_f32 v[26:27], v[26:27], 1.0 op_sel_hi:[1,0]
	s_waitcnt vmcnt(26)
	v_mov_b32_e32 v94, v174
	v_mov_b32_e32 v95, v175
	v_mov_b32_e32 v96, v176
	v_mov_b32_e32 v97, v177
	global_load_dwordx4 v[174:177], v185, s[56:57]
	v_pk_fma_f32 v[34:35], v[24:25], v[28:29], v[96:97]
	v_pk_fma_f32 v[36:37], v[22:23], v[26:27], v[94:95]
	v_cvt_pk_bf16_f32 v23, v34, v35
	v_cvt_pk_bf16_f32 v22, v36, v37
	global_store_dwordx2 v[100:101], v[22:23], off offset:2048
	s_nop 0
	v_mul_f32_e32 v4, 0x45800000, v2
	v_cndmask_b32_e32 v2, v2, v4, vcc
	v_pk_mul_f32 v[70:71], v[2:3], v[70:71] op_sel_hi:[0,1]
	v_pk_mul_f32 v[62:63], v[2:3], v[62:63] op_sel_hi:[0,1]
	v_pk_mul_f32 v[56:57], v[2:3], v[56:57] op_sel_hi:[0,1]
	v_pk_mul_f32 v[52:53], v[2:3], v[52:53] op_sel_hi:[0,1]
	v_pk_mul_f32 v[82:83], v[2:3], v[82:83] op_sel_hi:[0,1]
	v_mov_b32_e32 v4, v7
	v_pk_mul_f32 v[50:51], v[2:3], v[50:51] op_sel_hi:[0,1]
	v_pk_mul_f32 v[4:5], v[2:3], v[4:5] op_sel_hi:[0,1]
	s_waitcnt vmcnt(27)
	v_mov_b32_e32 v22, v214
	v_mov_b32_e32 v23, v215
	v_mov_b32_e32 v24, v216
	v_mov_b32_e32 v25, v217
	global_load_dwordx4 v[214:217], v185, s[54:55]
	v_pk_mul_f32 v[22:23], v[88:89], v[22:23]
	v_pk_mul_f32 v[24:25], v[90:91], v[24:25]
	s_waitcnt vmcnt(27)
	v_mov_b32_e32 v26, v224
	v_mov_b32_e32 v27, v225
	v_mov_b32_e32 v28, v226
	v_mov_b32_e32 v29, v227
	global_load_dwordx4 v[224:227], v186, s[52:53]
	v_pk_add_f32 v[28:29], v[28:29], 1.0 op_sel_hi:[1,0]
	v_pk_add_f32 v[88:89], v[26:27], 1.0 op_sel_hi:[1,0]
	s_waitcnt vmcnt(27)
	v_mov_b32_e32 v94, v228
	v_mov_b32_e32 v95, v229
	v_mov_b32_e32 v96, v230
	v_mov_b32_e32 v97, v231
	global_load_dwordx4 v[228:231], v186, s[56:57]
	v_pk_fma_f32 v[26:27], v[24:25], v[28:29], v[96:97]
	v_pk_fma_f32 v[28:29], v[22:23], v[88:89], v[94:95]
	v_cvt_pk_bf16_f32 v23, v26, v27
	v_cvt_pk_bf16_f32 v22, v28, v29
	global_store_dwordx2 v[100:101], v[22:23], off offset:2560
	s_nop 0
	v_lshl_add_u64 v[96:97], v[12:13], 0, s[50:51]
	s_waitcnt vmcnt(28)
	v_mov_b32_e32 v22, v232
	v_mov_b32_e32 v23, v233
	v_mov_b32_e32 v24, v234
	v_mov_b32_e32 v25, v235
	global_load_dwordx4 v[232:235], v186, s[54:55]
	v_pk_mul_f32 v[78:79], v[78:79], v[22:23]
	v_pk_mul_f32 v[22:23], v[80:81], v[24:25]
	s_waitcnt vmcnt(28)
	v_mov_b32_e32 v88, v236
	v_mov_b32_e32 v89, v237
	v_mov_b32_e32 v90, v238
	v_mov_b32_e32 v91, v239
	global_load_dwordx4 v[236:239], v187, s[52:53]
	v_pk_add_f32 v[24:25], v[90:91], 1.0 op_sel_hi:[1,0]
	v_pk_add_f32 v[80:81], v[88:89], 1.0 op_sel_hi:[1,0]
	s_waitcnt vmcnt(28)
	v_mov_b32_e32 v92, v240
	v_mov_b32_e32 v93, v241
	v_mov_b32_e32 v94, v242
	v_mov_b32_e32 v95, v243
	global_load_dwordx4 v[240:243], v187, s[56:57]
	v_pk_fma_f32 v[22:23], v[22:23], v[24:25], v[94:95]
	v_pk_fma_f32 v[24:25], v[78:79], v[80:81], v[92:93]
	v_cvt_pk_bf16_f32 v79, v22, v23
	v_cvt_pk_bf16_f32 v78, v24, v25
	global_store_dwordx2 v[100:101], v[78:79], off offset:3072
	s_nop 0
	s_waitcnt vmcnt(29)
	v_mov_b32_e32 v78, v244
	v_mov_b32_e32 v79, v245
	v_mov_b32_e32 v80, v246
	v_mov_b32_e32 v81, v247
	global_load_dwordx4 v[244:247], v187, s[54:55]
	v_pk_mul_f32 v[20:21], v[18:19], v[78:79]
	v_pk_mul_f32 v[18:19], v[58:59], v[80:81]
	s_waitcnt vmcnt(29)
	v_mov_b32_e32 v88, v248
	v_mov_b32_e32 v89, v249
	v_mov_b32_e32 v90, v250
	v_mov_b32_e32 v91, v251
	global_load_dwordx4 v[248:251], v190, s[52:53]
	v_pk_add_f32 v[58:59], v[90:91], 1.0 op_sel_hi:[1,0]
	v_pk_add_f32 v[78:79], v[88:89], 1.0 op_sel_hi:[1,0]
	s_waitcnt vmcnt(29)
	v_mov_b32_e32 v92, v118
	v_mov_b32_e32 v93, v119
	v_mov_b32_e32 v94, v120
	v_mov_b32_e32 v95, v121
	global_load_dwordx4 v[118:121], v190, s[56:57]
	v_pk_fma_f32 v[18:19], v[18:19], v[58:59], v[94:95]
	v_pk_fma_f32 v[20:21], v[20:21], v[78:79], v[92:93]
	v_cvt_pk_bf16_f32 v59, v18, v19
	v_cvt_pk_bf16_f32 v58, v20, v21
	global_store_dwordx2 v[100:101], v[58:59], off offset:3584
	v_pk_mul_f32 v[58:59], v[2:3], v[72:73] op_sel_hi:[0,1]
	s_waitcnt vmcnt(30)
	v_mov_b32_e32 v78, v122
	v_mov_b32_e32 v79, v123
	v_mov_b32_e32 v80, v124
	v_mov_b32_e32 v81, v125
	global_load_dwordx4 v[122:125], v190, s[54:55]
	v_pk_mul_f32 v[72:73], v[78:79], v[70:71]
	v_pk_mul_f32 v[58:59], v[80:81], v[58:59]
	s_waitcnt vmcnt(30)
	v_mov_b32_e32 v88, v126
	v_mov_b32_e32 v89, v127
	v_mov_b32_e32 v90, v128
	v_mov_b32_e32 v91, v129
	v_pk_add_f32 v[70:71], v[90:91], 1.0 op_sel_hi:[1,0]
	v_pk_add_f32 v[78:79], v[88:89], 1.0 op_sel_hi:[1,0]
	s_waitcnt vmcnt(28)
	v_mov_b32_e32 v92, v130
	v_mov_b32_e32 v93, v131
	v_mov_b32_e32 v94, v132
	v_mov_b32_e32 v95, v133
	v_pk_fma_f32 v[70:71], v[70:71], v[58:59], v[94:95]
	v_pk_fma_f32 v[72:73], v[78:79], v[72:73], v[92:93]
	v_cvt_pk_bf16_f32 v59, v70, v71
	v_cvt_pk_bf16_f32 v58, v72, v73
	global_store_dwordx2 v[96:97], v[58:59], off
	v_mov_b32_e32 v58, v75
	v_mov_b32_e32 v59, v77
	v_mov_b32_e32 v75, v76
	v_pk_mul_f32 v[58:59], v[2:3], v[58:59] op_sel_hi:[0,1]
	v_pk_mul_f32 v[74:75], v[2:3], v[74:75] op_sel_hi:[0,1]
	s_waitcnt vmcnt(28)
	v_mov_b32_e32 v78, v134
	v_mov_b32_e32 v79, v135
	v_mov_b32_e32 v80, v136
	v_mov_b32_e32 v81, v137
	v_pk_mul_f32 v[74:75], v[78:79], v[74:75]
	v_pk_mul_f32 v[58:59], v[80:81], v[58:59]
	s_waitcnt vmcnt(27)
	v_mov_b32_e32 v88, v138
	v_mov_b32_e32 v89, v139
	v_mov_b32_e32 v90, v140
	v_mov_b32_e32 v91, v141
	v_pk_add_f32 v[76:77], v[90:91], 1.0 op_sel_hi:[1,0]
	v_pk_add_f32 v[80:81], v[88:89], 1.0 op_sel_hi:[1,0]
	s_waitcnt vmcnt(25)
	v_mov_b32_e32 v92, v142
	v_mov_b32_e32 v93, v143
	v_mov_b32_e32 v94, v144
	v_mov_b32_e32 v95, v145
	v_pk_fma_f32 v[78:79], v[76:77], v[58:59], v[94:95]
	v_pk_fma_f32 v[80:81], v[80:81], v[74:75], v[92:93]
	v_cvt_pk_bf16_f32 v59, v78, v79
	v_cvt_pk_bf16_f32 v58, v80, v81
	global_store_dwordx2 v[96:97], v[58:59], off offset:512
	v_pk_mul_f32 v[58:59], v[2:3], v[64:65] op_sel_hi:[0,1]
	s_waitcnt vmcnt(25)
	v_mov_b32_e32 v74, v146
	v_mov_b32_e32 v75, v147
	v_mov_b32_e32 v76, v148
	v_mov_b32_e32 v77, v149
	v_pk_mul_f32 v[62:63], v[74:75], v[62:63]
	v_pk_mul_f32 v[58:59], v[76:77], v[58:59]
	s_waitcnt vmcnt(24)
	v_mov_b32_e32 v88, v150
	v_mov_b32_e32 v89, v151
	v_mov_b32_e32 v90, v152
	v_mov_b32_e32 v91, v153
	v_pk_add_f32 v[64:65], v[90:91], 1.0 op_sel_hi:[1,0]
	v_pk_add_f32 v[76:77], v[88:89], 1.0 op_sel_hi:[1,0]
	s_waitcnt vmcnt(22)
	v_mov_b32_e32 v92, v154
	v_mov_b32_e32 v93, v155
	v_mov_b32_e32 v94, v156
	v_mov_b32_e32 v95, v157
	v_pk_fma_f32 v[74:75], v[64:65], v[58:59], v[94:95]
	v_pk_fma_f32 v[76:77], v[76:77], v[62:63], v[92:93]
	v_cvt_pk_bf16_f32 v59, v74, v75
	v_cvt_pk_bf16_f32 v58, v76, v77
	global_store_dwordx2 v[96:97], v[58:59], off offset:1024
	s_waitcnt vmcnt(22)
	v_mov_b32_e32 v62, v158
	v_mov_b32_e32 v63, v159
	v_mov_b32_e32 v64, v160
	v_mov_b32_e32 v65, v161
	v_pk_mul_f32 v[52:53], v[52:53], v[62:63]
	v_pk_mul_f32 v[54:55], v[56:57], v[64:65]
	s_waitcnt vmcnt(21)
	v_mov_b32_e32 v88, v162
	v_mov_b32_e32 v89, v163
	v_mov_b32_e32 v90, v164
	v_mov_b32_e32 v91, v165
	v_pk_add_f32 v[56:57], v[90:91], 1.0 op_sel_hi:[1,0]
	v_pk_add_f32 v[58:59], v[88:89], 1.0 op_sel_hi:[1,0]
	s_waitcnt vmcnt(19)
	v_mov_b32_e32 v92, v166
	v_mov_b32_e32 v93, v167
	v_mov_b32_e32 v94, v168
	v_mov_b32_e32 v95, v169
	v_pk_fma_f32 v[62:63], v[54:55], v[56:57], v[94:95]
	v_pk_fma_f32 v[64:65], v[52:53], v[58:59], v[92:93]
	v_cvt_pk_bf16_f32 v53, v62, v63
	v_cvt_pk_bf16_f32 v52, v64, v65
	global_store_dwordx2 v[96:97], v[52:53], off offset:1536
	s_nop 0
	v_mov_b32_e32 v92, v67
	v_mov_b32_e32 v93, v69
	v_mov_b32_e32 v67, v68
	v_pk_mul_f32 v[92:93], v[2:3], v[92:93] op_sel_hi:[0,1]
	v_pk_mul_f32 v[66:67], v[2:3], v[66:67] op_sel_hi:[0,1]
	s_waitcnt vmcnt(19)
	v_mov_b32_e32 v52, v170
	v_mov_b32_e32 v53, v171
	v_mov_b32_e32 v54, v172
	v_mov_b32_e32 v55, v173
	v_pk_mul_f32 v[52:53], v[66:67], v[52:53]
	v_pk_mul_f32 v[54:55], v[92:93], v[54:55]
	s_waitcnt vmcnt(18)
	v_mov_b32_e32 v56, v174
	v_mov_b32_e32 v57, v175
	v_mov_b32_e32 v58, v176
	v_mov_b32_e32 v59, v177
	v_pk_add_f32 v[58:59], v[58:59], 1.0 op_sel_hi:[1,0]
	v_pk_add_f32 v[56:57], v[56:57], 1.0 op_sel_hi:[1,0]
	s_waitcnt vmcnt(16)
	v_mov_b32_e32 v88, v214
	v_mov_b32_e32 v89, v215
	v_mov_b32_e32 v90, v216
	v_mov_b32_e32 v91, v217
	v_pk_fma_f32 v[66:67], v[54:55], v[58:59], v[90:91]
	v_pk_fma_f32 v[68:69], v[52:53], v[56:57], v[88:89]
	v_cvt_pk_bf16_f32 v53, v66, v67
	v_cvt_pk_bf16_f32 v52, v68, v69
	global_store_dwordx2 v[96:97], v[52:53], off offset:2048
	s_nop 0
	v_mov_b32_e32 v92, v61
	v_mov_b32_e32 v93, v87
	v_mov_b32_e32 v61, v86
	v_pk_mul_f32 v[92:93], v[2:3], v[92:93] op_sel_hi:[0,1]
	v_pk_mul_f32 v[60:61], v[2:3], v[60:61] op_sel_hi:[0,1]
	s_waitcnt vmcnt(16)
	v_mov_b32_e32 v52, v224
	v_mov_b32_e32 v53, v225
	v_mov_b32_e32 v54, v226
	v_mov_b32_e32 v55, v227
	v_pk_mul_f32 v[52:53], v[60:61], v[52:53]
	v_pk_mul_f32 v[54:55], v[92:93], v[54:55]
	s_waitcnt vmcnt(15)
	v_mov_b32_e32 v56, v228
	v_mov_b32_e32 v57, v229
	v_mov_b32_e32 v58, v230
	v_mov_b32_e32 v59, v231
	v_pk_add_f32 v[58:59], v[58:59], 1.0 op_sel_hi:[1,0]
	v_pk_add_f32 v[56:57], v[56:57], 1.0 op_sel_hi:[1,0]
	s_waitcnt vmcnt(13)
	v_mov_b32_e32 v88, v232
	v_mov_b32_e32 v89, v233
	v_mov_b32_e32 v90, v234
	v_mov_b32_e32 v91, v235
	v_pk_fma_f32 v[58:59], v[54:55], v[58:59], v[90:91]
	v_pk_fma_f32 v[60:61], v[52:53], v[56:57], v[88:89]
	v_cvt_pk_bf16_f32 v53, v58, v59
	v_cvt_pk_bf16_f32 v52, v60, v61
	global_store_dwordx2 v[96:97], v[52:53], off offset:2560
	s_nop 0
	v_pk_mul_f32 v[56:57], v[2:3], v[84:85] op_sel_hi:[0,1]
	s_waitcnt vmcnt(13)
	v_mov_b32_e32 v52, v236
	v_mov_b32_e32 v53, v237
	v_mov_b32_e32 v54, v238
	v_mov_b32_e32 v55, v239
	v_pk_mul_f32 v[52:53], v[82:83], v[52:53]
	v_pk_mul_f32 v[54:55], v[56:57], v[54:55]
	s_waitcnt vmcnt(12)
	v_mov_b32_e32 v86, v240
	v_mov_b32_e32 v87, v241
	v_mov_b32_e32 v88, v242
	v_mov_b32_e32 v89, v243
	v_pk_add_f32 v[56:57], v[88:89], 1.0 op_sel_hi:[1,0]
	v_pk_add_f32 v[82:83], v[86:87], 1.0 op_sel_hi:[1,0]
	s_waitcnt vmcnt(10)
	v_mov_b32_e32 v90, v244
	v_mov_b32_e32 v91, v245
	v_mov_b32_e32 v92, v246
	v_mov_b32_e32 v93, v247
	v_pk_fma_f32 v[54:55], v[54:55], v[56:57], v[92:93]
	v_pk_fma_f32 v[56:57], v[52:53], v[82:83], v[90:91]
	v_cvt_pk_bf16_f32 v53, v54, v55
	v_cvt_pk_bf16_f32 v52, v56, v57
	global_store_dwordx2 v[96:97], v[52:53], off offset:3072
	s_waitcnt vmcnt(10)
	v_mov_b32_e32 v82, v248
	v_mov_b32_e32 v83, v249
	v_mov_b32_e32 v84, v250
	v_mov_b32_e32 v85, v251
	v_pk_mul_f32 v[4:5], v[4:5], v[82:83]
	v_pk_mul_f32 v[6:7], v[50:51], v[84:85]
	s_waitcnt vmcnt(9)
	v_mov_b32_e32 v86, v118
	v_mov_b32_e32 v87, v119
	v_mov_b32_e32 v88, v120
	v_mov_b32_e32 v89, v121
	v_pk_add_f32 v[50:51], v[88:89], 1.0 op_sel_hi:[1,0]
	v_pk_add_f32 v[52:53], v[86:87], 1.0 op_sel_hi:[1,0]
	s_waitcnt vmcnt(7)
	v_mov_b32_e32 v90, v122
	v_mov_b32_e32 v91, v123
	v_mov_b32_e32 v92, v124
	v_mov_b32_e32 v93, v125
	v_pk_fma_f32 v[50:51], v[6:7], v[50:51], v[92:93]
	v_pk_fma_f32 v[52:53], v[4:5], v[52:53], v[90:91]
	v_cvt_pk_bf16_f32 v5, v50, v51
	v_cvt_pk_bf16_f32 v4, v52, v53
	global_store_dwordx2 v[96:97], v[4:5], off offset:3584
	v_add_u32_e32 v118, 0x10400, v110
	v_add_u32_e32 v119, 0x10800, v110
	v_add_u32_e32 v120, 0x10c00, v110
	v_add_u32_e32 v121, 0x11000, v110
	v_add_u32_e32 v122, 0x11400, v110
	v_add_u32_e32 v123, 0x11800, v110
	v_add_u32_e32 v124, 0x11c00, v110
	v_add_u32_e32 v125, 0x12000, v110
	v_add_u32_e32 v126, 0x12400, v110
	v_add_u32_e32 v127, 0x12800, v110
	v_add_u32_e32 v128, 0x12c00, v110
	v_add_u32_e32 v129, 0x13000, v110
	v_add_u32_e32 v130, 0x13400, v110
	v_add_u32_e32 v131, 0x13800, v110
	v_add_u32_e32 v132, 0x13c00, v110
	v_add_u32_e32 v133, 0x14000, v110
	v_add_u32_e32 v134, 0x14400, v110
	v_add_u32_e32 v135, 0x14800, v110
	v_add_u32_e32 v136, 0x14c00, v110
	v_add_u32_e32 v137, 0x15000, v110
	v_add_u32_e32 v138, 0x15400, v110
	v_add_u32_e32 v139, 0x15800, v110
	v_add_u32_e32 v140, 0x15c00, v110
	v_add_u32_e32 v141, 0x16000, v110
	v_add_u32_e32 v142, 0x16400, v110
	v_add_u32_e32 v143, 0x16800, v110
	v_add_u32_e32 v144, 0x16c00, v110
	v_add_u32_e32 v145, 0x17000, v110
	v_add_u32_e32 v146, 0x17400, v110
	v_add_u32_e32 v147, 0x17800, v110
	v_add_u32_e32 v148, 0x17c00, v110
	v_add_u32_e32 v149, 0x18000, v110
	v_add_u32_e32 v150, 0x18400, v110
	v_add_u32_e32 v151, 0x18800, v110
	v_add_u32_e32 v152, 0x18c00, v110
	v_add_u32_e32 v153, 0x19000, v110
	v_add_u32_e32 v154, 0x19400, v110
	v_add_u32_e32 v155, 0x19800, v110
	v_add_u32_e32 v156, 0x19c00, v110
	v_add_u32_e32 v157, 0x1a000, v110
	v_add_u32_e32 v158, 0x1a400, v110
	v_add_u32_e32 v159, 0x1a800, v110
	v_add_u32_e32 v160, 0x1ac00, v110
	v_add_u32_e32 v161, 0x1b000, v110
	v_add_u32_e32 v162, 0x1b400, v110
	v_add_u32_e32 v163, 0x1b800, v110
	v_add_u32_e32 v164, 0x1bc00, v110
	v_add_u32_e32 v165, 0x1c000, v110
	v_add_u32_e32 v166, 0x1c400, v110
	v_add_u32_e32 v167, 0x1c800, v110
	v_add_u32_e32 v168, 0x1cc00, v110
	v_add_u32_e32 v169, 0x1d000, v110
	v_add_u32_e32 v170, 0x1d400, v110
	v_add_u32_e32 v171, 0x1d800, v110
	v_add_u32_e32 v172, 0x1dc00, v110
	v_add_u32_e32 v173, 0x1e000, v110
	v_add_u32_e32 v174, 0x1e400, v110
	v_add_u32_e32 v175, 0x1e800, v110
	v_add_u32_e32 v176, 0x1ec00, v110
	v_add_u32_e32 v177, 0x1f000, v110
	ds_read_b128 v[4:7], v110
	s_waitcnt lgkmcnt(0)
	v_mul_f32_e32 v2, v5, v49
	v_mul_f32_e32 v5, v5, v73
	v_fmac_f32_e32 v2, v4, v48
	v_fmac_f32_e32 v5, v4, v72
	v_mul_f32_e32 v4, v7, v71
	v_mul_f32_e32 v82, v7, v47
	v_fmac_f32_e32 v4, v6, v70
	v_fmac_f32_e32 v82, v6, v46
	v_add_f32_e32 v4, v5, v4
	v_add_f32_e32 v2, v2, v82
	v_add_f32_e32 v82, 0, v4
	ds_read_b128 v[4:7], v110 offset:1024
	v_add_f32_e32 v2, 0, v2
	s_waitcnt lgkmcnt(0)
	v_mul_f32_e32 v83, v5, v45
	v_mul_f32_e32 v5, v5, v81
	v_fmac_f32_e32 v83, v4, v44
	v_fmac_f32_e32 v5, v4, v80
	v_mul_f32_e32 v4, v7, v79
	v_fmac_f32_e32 v4, v6, v78
	v_mul_f32_e32 v84, v7, v43
	v_add_f32_e32 v4, v5, v4
	v_fmac_f32_e32 v84, v6, v42
	v_add_f32_e32 v82, v82, v4
	ds_read_b128 v[4:7], v110 offset:2048
	v_add_f32_e32 v83, v83, v84
	v_add_f32_e32 v2, v2, v83
	s_waitcnt lgkmcnt(0)
	v_mul_f32_e32 v83, v5, v41
	v_mul_f32_e32 v5, v5, v77
	v_fmac_f32_e32 v83, v4, v40
	v_fmac_f32_e32 v5, v4, v76
	v_mul_f32_e32 v4, v7, v75
	v_fmac_f32_e32 v4, v6, v74
	v_mul_f32_e32 v84, v7, v39
	v_add_f32_e32 v4, v5, v4
	v_fmac_f32_e32 v84, v6, v38
	v_add_f32_e32 v82, v82, v4
	ds_read_b128 v[4:7], v110 offset:3072
	v_add_f32_e32 v83, v83, v84
	v_add_f32_e32 v2, v2, v83
	s_waitcnt lgkmcnt(0)
	v_mul_f32_e32 v83, v5, v33
	v_mul_f32_e32 v5, v5, v65
	v_fmac_f32_e32 v83, v4, v32
	v_fmac_f32_e32 v5, v4, v64
	v_mul_f32_e32 v4, v7, v63
	v_fmac_f32_e32 v4, v6, v62
	v_mul_f32_e32 v84, v7, v31
	v_add_f32_e32 v4, v5, v4
	v_fmac_f32_e32 v84, v6, v30
	v_add_f32_e32 v82, v82, v4
	ds_read_b128 v[4:7], v110 offset:4096
	v_add_f32_e32 v83, v83, v84
	v_add_f32_e32 v2, v2, v83
	s_waitcnt lgkmcnt(0)
	v_mul_f32_e32 v83, v5, v37
	v_mul_f32_e32 v5, v5, v69
	v_fmac_f32_e32 v83, v4, v36
	v_fmac_f32_e32 v5, v4, v68
	v_mul_f32_e32 v4, v7, v67
	v_fmac_f32_e32 v4, v6, v66
	v_mul_f32_e32 v84, v7, v35
	v_add_f32_e32 v4, v5, v4
	v_fmac_f32_e32 v84, v6, v34
	v_add_f32_e32 v82, v82, v4
	ds_read_b128 v[4:7], v110 offset:5120
	v_add_f32_e32 v83, v83, v84
	v_add_f32_e32 v2, v2, v83
	s_waitcnt lgkmcnt(0)
	v_mul_f32_e32 v83, v5, v29
	v_mul_f32_e32 v5, v5, v61
	v_fmac_f32_e32 v83, v4, v28
	v_fmac_f32_e32 v5, v4, v60
	v_mul_f32_e32 v4, v7, v59
	v_fmac_f32_e32 v4, v6, v58
	v_mul_f32_e32 v84, v7, v27
	v_add_f32_e32 v4, v5, v4
	v_fmac_f32_e32 v84, v6, v26
	v_add_f32_e32 v82, v82, v4
	ds_read_b128 v[4:7], v110 offset:6144
	v_add_f32_e32 v83, v83, v84
	v_add_f32_e32 v2, v2, v83
	s_waitcnt lgkmcnt(0)
	v_mul_f32_e32 v83, v5, v25
	v_mul_f32_e32 v5, v5, v57
	v_fmac_f32_e32 v83, v4, v24
	v_fmac_f32_e32 v5, v4, v56
	v_mul_f32_e32 v4, v7, v55
	v_fmac_f32_e32 v4, v6, v54
	v_mul_f32_e32 v84, v7, v23
	v_add_f32_e32 v4, v5, v4
	v_fmac_f32_e32 v84, v6, v22
	v_add_f32_e32 v82, v82, v4
	ds_read_b128 v[4:7], v110 offset:7168
	v_add_f32_e32 v83, v83, v84
	v_add_f32_e32 v2, v2, v83
	s_waitcnt lgkmcnt(0)
	v_mul_f32_e32 v83, v5, v21
	v_mul_f32_e32 v5, v5, v53
	v_fmac_f32_e32 v83, v4, v20
	v_fmac_f32_e32 v5, v4, v52
	v_mul_f32_e32 v4, v7, v51
	v_fmac_f32_e32 v4, v6, v50
	v_mul_f32_e32 v84, v7, v19
	v_add_f32_e32 v4, v5, v4
	v_fmac_f32_e32 v84, v6, v18
	v_add_f32_e32 v82, v82, v4
	ds_read_b128 v[4:7], v110 offset:8192
	v_add_f32_e32 v83, v83, v84
	v_add_f32_e32 v2, v2, v83
	s_waitcnt lgkmcnt(0)
	v_mul_f32_e32 v83, v5, v49
	v_mul_f32_e32 v5, v5, v73
	v_fmac_f32_e32 v83, v4, v48
	v_fmac_f32_e32 v5, v4, v72
	v_mul_f32_e32 v4, v7, v71
	v_mul_f32_e32 v84, v7, v47
	v_fmac_f32_e32 v4, v6, v70
	v_fmac_f32_e32 v84, v6, v46
	v_add_f32_e32 v4, v5, v4
	v_add_f32_e32 v83, v83, v84
	v_add_f32_e32 v84, 0, v4
	ds_read_b128 v[4:7], v110 offset:9216
	v_add_f32_e32 v83, 0, v83
	s_waitcnt lgkmcnt(0)
	v_mul_f32_e32 v85, v5, v45
	v_mul_f32_e32 v5, v5, v81
	v_fmac_f32_e32 v85, v4, v44
	v_fmac_f32_e32 v5, v4, v80
	v_mul_f32_e32 v4, v7, v79
	v_fmac_f32_e32 v4, v6, v78
	v_mul_f32_e32 v86, v7, v43
	v_add_f32_e32 v4, v5, v4
	v_fmac_f32_e32 v86, v6, v42
	v_add_f32_e32 v84, v84, v4
	ds_read_b128 v[4:7], v110 offset:10240
	v_add_f32_e32 v85, v85, v86
	v_add_f32_e32 v83, v83, v85
	s_waitcnt lgkmcnt(0)
	v_mul_f32_e32 v85, v5, v41
	v_mul_f32_e32 v5, v5, v77
	v_fmac_f32_e32 v85, v4, v40
	v_fmac_f32_e32 v5, v4, v76
	v_mul_f32_e32 v4, v7, v75
	v_fmac_f32_e32 v4, v6, v74
	v_mul_f32_e32 v86, v7, v39
	v_add_f32_e32 v4, v5, v4
	v_fmac_f32_e32 v86, v6, v38
	v_add_f32_e32 v84, v84, v4
	ds_read_b128 v[4:7], v110 offset:11264
	v_add_f32_e32 v85, v85, v86
	v_add_f32_e32 v83, v83, v85
	s_waitcnt lgkmcnt(0)
	v_mul_f32_e32 v85, v5, v33
	v_mul_f32_e32 v5, v5, v65
	v_fmac_f32_e32 v85, v4, v32
	v_fmac_f32_e32 v5, v4, v64
	v_mul_f32_e32 v4, v7, v63
	v_fmac_f32_e32 v4, v6, v62
	v_mul_f32_e32 v86, v7, v31
	v_add_f32_e32 v4, v5, v4
	v_fmac_f32_e32 v86, v6, v30
	v_add_f32_e32 v84, v84, v4
	ds_read_b128 v[4:7], v110 offset:12288
	v_add_f32_e32 v85, v85, v86
	v_add_f32_e32 v83, v83, v85
	s_waitcnt lgkmcnt(0)
	v_mul_f32_e32 v85, v5, v37
	v_mul_f32_e32 v5, v5, v69
	v_fmac_f32_e32 v85, v4, v36
	v_fmac_f32_e32 v5, v4, v68
	v_mul_f32_e32 v4, v7, v67
	v_fmac_f32_e32 v4, v6, v66
	v_mul_f32_e32 v86, v7, v35
	v_add_f32_e32 v4, v5, v4
	v_fmac_f32_e32 v86, v6, v34
	v_add_f32_e32 v84, v84, v4
	ds_read_b128 v[4:7], v110 offset:13312
	v_add_f32_e32 v85, v85, v86
	v_add_f32_e32 v83, v83, v85
	s_waitcnt lgkmcnt(0)
	v_mul_f32_e32 v85, v5, v29
	v_mul_f32_e32 v5, v5, v61
	v_fmac_f32_e32 v85, v4, v28
	v_fmac_f32_e32 v5, v4, v60
	v_mul_f32_e32 v4, v7, v59
	v_fmac_f32_e32 v4, v6, v58
	v_mul_f32_e32 v86, v7, v27
	v_add_f32_e32 v4, v5, v4
	v_fmac_f32_e32 v86, v6, v26
	v_add_f32_e32 v84, v84, v4
	ds_read_b128 v[4:7], v110 offset:14336
	v_add_f32_e32 v85, v85, v86
	v_add_f32_e32 v83, v83, v85
	s_waitcnt lgkmcnt(0)
	v_mul_f32_e32 v85, v5, v25
	v_mul_f32_e32 v5, v5, v57
	v_fmac_f32_e32 v85, v4, v24
	v_fmac_f32_e32 v5, v4, v56
	v_mul_f32_e32 v4, v7, v55
	v_fmac_f32_e32 v4, v6, v54
	v_mul_f32_e32 v86, v7, v23
	v_add_f32_e32 v4, v5, v4
	v_fmac_f32_e32 v86, v6, v22
	v_add_f32_e32 v84, v84, v4
	ds_read_b128 v[4:7], v110 offset:15360
	v_add_f32_e32 v85, v85, v86
	v_add_f32_e32 v83, v83, v85
	s_waitcnt lgkmcnt(0)
	v_mul_f32_e32 v85, v5, v21
	v_mul_f32_e32 v5, v5, v53
	v_fmac_f32_e32 v85, v4, v20
	v_fmac_f32_e32 v5, v4, v52
	v_mul_f32_e32 v4, v7, v51
	v_fmac_f32_e32 v4, v6, v50
	v_mul_f32_e32 v86, v7, v19
	v_add_f32_e32 v4, v5, v4
	v_fmac_f32_e32 v86, v6, v18
	v_add_f32_e32 v84, v84, v4
	ds_read_b128 v[4:7], v110 offset:16384
	v_add_f32_e32 v85, v85, v86
	v_add_f32_e32 v83, v83, v85
	s_waitcnt lgkmcnt(0)
	v_mul_f32_e32 v85, v5, v49
	v_mul_f32_e32 v5, v5, v73
	v_fmac_f32_e32 v85, v4, v48
	v_fmac_f32_e32 v5, v4, v72
	v_mul_f32_e32 v4, v7, v71
	v_mul_f32_e32 v86, v7, v47
	v_fmac_f32_e32 v4, v6, v70
	v_fmac_f32_e32 v86, v6, v46
	v_add_f32_e32 v4, v5, v4
	v_add_f32_e32 v85, v85, v86
	v_add_f32_e32 v86, 0, v4
	ds_read_b128 v[4:7], v110 offset:17408
	v_add_f32_e32 v85, 0, v85
	s_waitcnt lgkmcnt(0)
	v_mul_f32_e32 v87, v5, v45
	v_mul_f32_e32 v5, v5, v81
	v_fmac_f32_e32 v87, v4, v44
	v_fmac_f32_e32 v5, v4, v80
	v_mul_f32_e32 v4, v7, v79
	v_fmac_f32_e32 v4, v6, v78
	v_mul_f32_e32 v88, v7, v43
	v_add_f32_e32 v4, v5, v4
	v_fmac_f32_e32 v88, v6, v42
	v_add_f32_e32 v86, v86, v4
	ds_read_b128 v[4:7], v110 offset:18432
	v_add_f32_e32 v87, v87, v88
	v_add_f32_e32 v85, v85, v87
	s_waitcnt lgkmcnt(0)
	v_mul_f32_e32 v87, v5, v41
	v_mul_f32_e32 v5, v5, v77
	v_fmac_f32_e32 v87, v4, v40
	v_fmac_f32_e32 v5, v4, v76
	v_mul_f32_e32 v4, v7, v75
	v_fmac_f32_e32 v4, v6, v74
	v_mul_f32_e32 v88, v7, v39
	v_add_f32_e32 v4, v5, v4
	v_fmac_f32_e32 v88, v6, v38
	v_add_f32_e32 v86, v86, v4
	ds_read_b128 v[4:7], v110 offset:19456
	v_add_f32_e32 v87, v87, v88
	v_add_f32_e32 v85, v85, v87
	s_waitcnt lgkmcnt(0)
	v_mul_f32_e32 v87, v5, v33
	v_mul_f32_e32 v5, v5, v65
	v_fmac_f32_e32 v87, v4, v32
	v_fmac_f32_e32 v5, v4, v64
	v_mul_f32_e32 v4, v7, v63
	v_fmac_f32_e32 v4, v6, v62
	v_mul_f32_e32 v88, v7, v31
	v_add_f32_e32 v4, v5, v4
	v_fmac_f32_e32 v88, v6, v30
	v_add_f32_e32 v86, v86, v4
	ds_read_b128 v[4:7], v110 offset:20480
	v_add_f32_e32 v87, v87, v88
	v_add_f32_e32 v85, v85, v87
	s_waitcnt lgkmcnt(0)
	v_mul_f32_e32 v87, v5, v37
	v_mul_f32_e32 v5, v5, v69
	v_fmac_f32_e32 v87, v4, v36
	v_fmac_f32_e32 v5, v4, v68
	v_mul_f32_e32 v4, v7, v67
	v_fmac_f32_e32 v4, v6, v66
	v_mul_f32_e32 v88, v7, v35
	v_add_f32_e32 v4, v5, v4
	v_fmac_f32_e32 v88, v6, v34
	v_add_f32_e32 v86, v86, v4
	ds_read_b128 v[4:7], v110 offset:21504
	v_add_f32_e32 v87, v87, v88
	v_add_f32_e32 v85, v85, v87
	s_waitcnt lgkmcnt(0)
	v_mul_f32_e32 v87, v5, v29
	v_mul_f32_e32 v5, v5, v61
	v_fmac_f32_e32 v87, v4, v28
	v_fmac_f32_e32 v5, v4, v60
	v_mul_f32_e32 v4, v7, v59
	v_fmac_f32_e32 v4, v6, v58
	v_mul_f32_e32 v88, v7, v27
	v_add_f32_e32 v4, v5, v4
	v_fmac_f32_e32 v88, v6, v26
	v_add_f32_e32 v86, v86, v4
	ds_read_b128 v[4:7], v110 offset:22528
	v_add_f32_e32 v87, v87, v88
	v_add_f32_e32 v85, v85, v87
	s_waitcnt lgkmcnt(0)
	v_mul_f32_e32 v87, v5, v25
	v_mul_f32_e32 v5, v5, v57
	v_fmac_f32_e32 v87, v4, v24
	v_fmac_f32_e32 v5, v4, v56
	v_mul_f32_e32 v4, v7, v55
	v_fmac_f32_e32 v4, v6, v54
	v_mul_f32_e32 v88, v7, v23
	v_add_f32_e32 v4, v5, v4
	v_fmac_f32_e32 v88, v6, v22
	v_add_f32_e32 v86, v86, v4
	ds_read_b128 v[4:7], v110 offset:23552
	v_add_f32_e32 v87, v87, v88
	v_add_f32_e32 v85, v85, v87
	s_waitcnt lgkmcnt(0)
	v_mul_f32_e32 v87, v5, v21
	v_mul_f32_e32 v5, v5, v53
	v_fmac_f32_e32 v87, v4, v20
	v_fmac_f32_e32 v5, v4, v52
	v_mul_f32_e32 v4, v7, v51
	v_fmac_f32_e32 v4, v6, v50
	v_mul_f32_e32 v88, v7, v19
	v_add_f32_e32 v4, v5, v4
	v_fmac_f32_e32 v88, v6, v18
	v_add_f32_e32 v86, v86, v4
	ds_read_b128 v[4:7], v110 offset:24576
	v_add_f32_e32 v87, v87, v88
	v_add_f32_e32 v85, v85, v87
	s_waitcnt lgkmcnt(0)
	v_mul_f32_e32 v87, v5, v49
	v_mul_f32_e32 v5, v5, v73
	v_fmac_f32_e32 v87, v4, v48
	v_fmac_f32_e32 v5, v4, v72
	v_mul_f32_e32 v4, v7, v71
	v_mul_f32_e32 v88, v7, v47
	v_fmac_f32_e32 v4, v6, v70
	v_fmac_f32_e32 v88, v6, v46
	v_add_f32_e32 v4, v5, v4
	v_add_f32_e32 v87, v87, v88
	v_add_f32_e32 v88, 0, v4
	ds_read_b128 v[4:7], v110 offset:25600
	v_add_f32_e32 v87, 0, v87
	s_waitcnt lgkmcnt(0)
	v_mul_f32_e32 v89, v5, v45
	v_mul_f32_e32 v5, v5, v81
	v_fmac_f32_e32 v89, v4, v44
	v_fmac_f32_e32 v5, v4, v80
	v_mul_f32_e32 v4, v7, v79
	v_fmac_f32_e32 v4, v6, v78
	v_mul_f32_e32 v90, v7, v43
	v_add_f32_e32 v4, v5, v4
	v_fmac_f32_e32 v90, v6, v42
	v_add_f32_e32 v88, v88, v4
	ds_read_b128 v[4:7], v110 offset:26624
	v_add_f32_e32 v89, v89, v90
	v_add_f32_e32 v87, v87, v89
	s_waitcnt lgkmcnt(0)
	v_mul_f32_e32 v89, v5, v41
	v_mul_f32_e32 v5, v5, v77
	v_fmac_f32_e32 v89, v4, v40
	v_fmac_f32_e32 v5, v4, v76
	v_mul_f32_e32 v4, v7, v75
	v_fmac_f32_e32 v4, v6, v74
	v_mul_f32_e32 v90, v7, v39
	v_add_f32_e32 v4, v5, v4
	v_fmac_f32_e32 v90, v6, v38
	v_add_f32_e32 v88, v88, v4
	ds_read_b128 v[4:7], v110 offset:27648
	v_add_f32_e32 v89, v89, v90
	v_add_f32_e32 v87, v87, v89
	s_waitcnt lgkmcnt(0)
	v_mul_f32_e32 v89, v5, v33
	v_mul_f32_e32 v5, v5, v65
	v_fmac_f32_e32 v89, v4, v32
	v_fmac_f32_e32 v5, v4, v64
	v_mul_f32_e32 v4, v7, v63
	v_fmac_f32_e32 v4, v6, v62
	v_mul_f32_e32 v90, v7, v31
	v_add_f32_e32 v4, v5, v4
	v_fmac_f32_e32 v90, v6, v30
	v_add_f32_e32 v88, v88, v4
	ds_read_b128 v[4:7], v110 offset:28672
	v_add_f32_e32 v89, v89, v90
	v_add_f32_e32 v87, v87, v89
	s_waitcnt lgkmcnt(0)
	v_mul_f32_e32 v89, v5, v37
	v_mul_f32_e32 v5, v5, v69
	v_fmac_f32_e32 v89, v4, v36
	v_fmac_f32_e32 v5, v4, v68
	v_mul_f32_e32 v4, v7, v67
	v_fmac_f32_e32 v4, v6, v66
	v_mul_f32_e32 v90, v7, v35
	v_add_f32_e32 v4, v5, v4
	v_fmac_f32_e32 v90, v6, v34
	v_add_f32_e32 v88, v88, v4
	ds_read_b128 v[4:7], v110 offset:29696
	v_add_f32_e32 v89, v89, v90
	v_add_f32_e32 v87, v87, v89
	s_waitcnt lgkmcnt(0)
	v_mul_f32_e32 v89, v5, v29
	v_mul_f32_e32 v5, v5, v61
	v_fmac_f32_e32 v89, v4, v28
	v_fmac_f32_e32 v5, v4, v60
	v_mul_f32_e32 v4, v7, v59
	v_fmac_f32_e32 v4, v6, v58
	v_mul_f32_e32 v90, v7, v27
	v_add_f32_e32 v4, v5, v4
	v_fmac_f32_e32 v90, v6, v26
	v_add_f32_e32 v88, v88, v4
	ds_read_b128 v[4:7], v110 offset:30720
	v_add_f32_e32 v89, v89, v90
	v_add_f32_e32 v87, v87, v89
	s_waitcnt lgkmcnt(0)
	v_mul_f32_e32 v89, v5, v25
	v_mul_f32_e32 v5, v5, v57
	v_fmac_f32_e32 v89, v4, v24
	v_fmac_f32_e32 v5, v4, v56
	v_mul_f32_e32 v4, v7, v55
	v_fmac_f32_e32 v4, v6, v54
	v_mul_f32_e32 v90, v7, v23
	v_add_f32_e32 v4, v5, v4
	v_fmac_f32_e32 v90, v6, v22
	v_add_f32_e32 v88, v88, v4
	ds_read_b128 v[4:7], v110 offset:31744
	v_add_f32_e32 v89, v89, v90
	v_add_f32_e32 v87, v87, v89
	s_waitcnt lgkmcnt(0)
	v_mul_f32_e32 v89, v5, v21
	v_mul_f32_e32 v5, v5, v53
	v_fmac_f32_e32 v89, v4, v20
	v_fmac_f32_e32 v5, v4, v52
	v_mul_f32_e32 v4, v7, v51
	v_fmac_f32_e32 v4, v6, v50
	v_mul_f32_e32 v90, v7, v19
	v_add_f32_e32 v4, v5, v4
	v_fmac_f32_e32 v90, v6, v18
	v_add_f32_e32 v88, v88, v4
	ds_read_b128 v[4:7], v110 offset:32768
	v_add_f32_e32 v89, v89, v90
	v_add_f32_e32 v87, v87, v89
	s_waitcnt lgkmcnt(0)
	v_mul_f32_e32 v89, v5, v49
	v_mul_f32_e32 v5, v5, v73
	v_fmac_f32_e32 v89, v4, v48
	v_fmac_f32_e32 v5, v4, v72
	v_mul_f32_e32 v4, v7, v71
	v_mul_f32_e32 v90, v7, v47
	v_fmac_f32_e32 v4, v6, v70
	v_fmac_f32_e32 v90, v6, v46
	v_add_f32_e32 v4, v5, v4
	v_add_f32_e32 v89, v89, v90
	v_add_f32_e32 v90, 0, v4
	ds_read_b128 v[4:7], v110 offset:33792
	v_add_f32_e32 v89, 0, v89
	s_waitcnt lgkmcnt(0)
	v_mul_f32_e32 v91, v5, v45
	v_mul_f32_e32 v5, v5, v81
	v_fmac_f32_e32 v91, v4, v44
	v_fmac_f32_e32 v5, v4, v80
	v_mul_f32_e32 v4, v7, v79
	v_fmac_f32_e32 v4, v6, v78
	v_mul_f32_e32 v92, v7, v43
	v_add_f32_e32 v4, v5, v4
	v_fmac_f32_e32 v92, v6, v42
	v_add_f32_e32 v90, v90, v4
	ds_read_b128 v[4:7], v110 offset:34816
	v_add_f32_e32 v91, v91, v92
	v_add_f32_e32 v89, v89, v91
	s_waitcnt lgkmcnt(0)
	v_mul_f32_e32 v91, v5, v41
	v_mul_f32_e32 v5, v5, v77
	v_fmac_f32_e32 v91, v4, v40
	v_fmac_f32_e32 v5, v4, v76
	v_mul_f32_e32 v4, v7, v75
	v_fmac_f32_e32 v4, v6, v74
	v_mul_f32_e32 v92, v7, v39
	v_add_f32_e32 v4, v5, v4
	v_fmac_f32_e32 v92, v6, v38
	v_add_f32_e32 v90, v90, v4
	ds_read_b128 v[4:7], v110 offset:35840
	v_add_f32_e32 v91, v91, v92
	v_add_f32_e32 v89, v89, v91
	s_waitcnt lgkmcnt(0)
	v_mul_f32_e32 v91, v5, v33
	v_mul_f32_e32 v5, v5, v65
	v_fmac_f32_e32 v91, v4, v32
	v_fmac_f32_e32 v5, v4, v64
	v_mul_f32_e32 v4, v7, v63
	v_fmac_f32_e32 v4, v6, v62
	v_mul_f32_e32 v92, v7, v31
	v_add_f32_e32 v4, v5, v4
	v_fmac_f32_e32 v92, v6, v30
	v_add_f32_e32 v90, v90, v4
	ds_read_b128 v[4:7], v110 offset:36864
	v_add_f32_e32 v91, v91, v92
	v_add_f32_e32 v89, v89, v91
	s_waitcnt lgkmcnt(0)
	v_mul_f32_e32 v91, v5, v37
	v_mul_f32_e32 v5, v5, v69
	v_fmac_f32_e32 v91, v4, v36
	v_fmac_f32_e32 v5, v4, v68
	v_mul_f32_e32 v4, v7, v67
	v_fmac_f32_e32 v4, v6, v66
	v_mul_f32_e32 v92, v7, v35
	v_add_f32_e32 v4, v5, v4
	v_fmac_f32_e32 v92, v6, v34
	v_add_f32_e32 v90, v90, v4
	ds_read_b128 v[4:7], v110 offset:37888
	v_add_f32_e32 v91, v91, v92
	v_add_f32_e32 v89, v89, v91
	s_waitcnt lgkmcnt(0)
	v_mul_f32_e32 v91, v5, v29
	v_mul_f32_e32 v5, v5, v61
	v_fmac_f32_e32 v91, v4, v28
	v_fmac_f32_e32 v5, v4, v60
	v_mul_f32_e32 v4, v7, v59
	v_fmac_f32_e32 v4, v6, v58
	v_mul_f32_e32 v92, v7, v27
	v_add_f32_e32 v4, v5, v4
	v_fmac_f32_e32 v92, v6, v26
	v_add_f32_e32 v90, v90, v4
	ds_read_b128 v[4:7], v110 offset:38912
	v_add_f32_e32 v91, v91, v92
	v_add_f32_e32 v89, v89, v91
	s_waitcnt lgkmcnt(0)
	v_mul_f32_e32 v91, v5, v25
	v_mul_f32_e32 v5, v5, v57
	v_fmac_f32_e32 v91, v4, v24
	v_fmac_f32_e32 v5, v4, v56
	v_mul_f32_e32 v4, v7, v55
	v_fmac_f32_e32 v4, v6, v54
	v_mul_f32_e32 v92, v7, v23
	v_add_f32_e32 v4, v5, v4
	v_fmac_f32_e32 v92, v6, v22
	v_add_f32_e32 v90, v90, v4
	ds_read_b128 v[4:7], v110 offset:39936
	v_add_f32_e32 v91, v91, v92
	v_add_f32_e32 v89, v89, v91
	s_waitcnt lgkmcnt(0)
	v_mul_f32_e32 v91, v5, v21
	v_mul_f32_e32 v5, v5, v53
	v_fmac_f32_e32 v91, v4, v20
	v_fmac_f32_e32 v5, v4, v52
	v_mul_f32_e32 v4, v7, v51
	v_fmac_f32_e32 v4, v6, v50
	v_mul_f32_e32 v92, v7, v19
	v_add_f32_e32 v4, v5, v4
	v_fmac_f32_e32 v92, v6, v18
	v_add_f32_e32 v90, v90, v4
	ds_read_b128 v[4:7], v110 offset:40960
	v_add_f32_e32 v91, v91, v92
	v_add_f32_e32 v89, v89, v91
	s_waitcnt lgkmcnt(0)
	v_mul_f32_e32 v91, v5, v49
	v_mul_f32_e32 v5, v5, v73
	v_fmac_f32_e32 v91, v4, v48
	v_fmac_f32_e32 v5, v4, v72
	v_mul_f32_e32 v4, v7, v71
	v_mul_f32_e32 v92, v7, v47
	v_fmac_f32_e32 v4, v6, v70
	v_fmac_f32_e32 v92, v6, v46
	v_add_f32_e32 v4, v5, v4
	v_add_f32_e32 v91, v91, v92
	v_add_f32_e32 v92, 0, v4
	ds_read_b128 v[4:7], v110 offset:41984
	v_add_f32_e32 v91, 0, v91
	s_waitcnt lgkmcnt(0)
	v_mul_f32_e32 v93, v5, v45
	v_mul_f32_e32 v5, v5, v81
	v_fmac_f32_e32 v93, v4, v44
	v_fmac_f32_e32 v5, v4, v80
	v_mul_f32_e32 v4, v7, v79
	v_fmac_f32_e32 v4, v6, v78
	v_mul_f32_e32 v94, v7, v43
	v_add_f32_e32 v4, v5, v4
	v_fmac_f32_e32 v94, v6, v42
	v_add_f32_e32 v92, v92, v4
	ds_read_b128 v[4:7], v110 offset:43008
	v_add_f32_e32 v93, v93, v94
	v_add_f32_e32 v91, v91, v93
	s_waitcnt lgkmcnt(0)
	v_mul_f32_e32 v93, v5, v41
	v_mul_f32_e32 v5, v5, v77
	v_fmac_f32_e32 v93, v4, v40
	v_fmac_f32_e32 v5, v4, v76
	v_mul_f32_e32 v4, v7, v75
	v_fmac_f32_e32 v4, v6, v74
	v_mul_f32_e32 v94, v7, v39
	v_add_f32_e32 v4, v5, v4
	v_fmac_f32_e32 v94, v6, v38
	v_add_f32_e32 v92, v92, v4
	ds_read_b128 v[4:7], v110 offset:44032
	v_add_f32_e32 v93, v93, v94
	v_add_f32_e32 v91, v91, v93
	s_waitcnt lgkmcnt(0)
	v_mul_f32_e32 v93, v5, v33
	v_mul_f32_e32 v5, v5, v65
	v_fmac_f32_e32 v93, v4, v32
	v_fmac_f32_e32 v5, v4, v64
	v_mul_f32_e32 v4, v7, v63
	v_fmac_f32_e32 v4, v6, v62
	v_mul_f32_e32 v94, v7, v31
	v_add_f32_e32 v4, v5, v4
	v_fmac_f32_e32 v94, v6, v30
	v_add_f32_e32 v92, v92, v4
	ds_read_b128 v[4:7], v110 offset:45056
	v_add_f32_e32 v93, v93, v94
	v_add_f32_e32 v91, v91, v93
	s_waitcnt lgkmcnt(0)
	v_mul_f32_e32 v93, v5, v37
	v_mul_f32_e32 v5, v5, v69
	v_fmac_f32_e32 v93, v4, v36
	v_fmac_f32_e32 v5, v4, v68
	v_mul_f32_e32 v4, v7, v67
	v_fmac_f32_e32 v4, v6, v66
	v_mul_f32_e32 v94, v7, v35
	v_add_f32_e32 v4, v5, v4
	v_fmac_f32_e32 v94, v6, v34
	v_add_f32_e32 v92, v92, v4
	ds_read_b128 v[4:7], v110 offset:46080
	v_add_f32_e32 v93, v93, v94
	v_add_f32_e32 v91, v91, v93
	s_waitcnt lgkmcnt(0)
	v_mul_f32_e32 v93, v5, v29
	v_mul_f32_e32 v5, v5, v61
	v_fmac_f32_e32 v93, v4, v28
	v_fmac_f32_e32 v5, v4, v60
	v_mul_f32_e32 v4, v7, v59
	v_fmac_f32_e32 v4, v6, v58
	v_mul_f32_e32 v94, v7, v27
	v_add_f32_e32 v4, v5, v4
	v_fmac_f32_e32 v94, v6, v26
	v_add_f32_e32 v92, v92, v4
	ds_read_b128 v[4:7], v110 offset:47104
	v_add_f32_e32 v93, v93, v94
	v_add_f32_e32 v91, v91, v93
	s_waitcnt lgkmcnt(0)
	v_mul_f32_e32 v93, v5, v25
	v_mul_f32_e32 v5, v5, v57
	v_fmac_f32_e32 v93, v4, v24
	v_fmac_f32_e32 v5, v4, v56
	v_mul_f32_e32 v4, v7, v55
	v_fmac_f32_e32 v4, v6, v54
	v_mul_f32_e32 v94, v7, v23
	v_add_f32_e32 v4, v5, v4
	v_fmac_f32_e32 v94, v6, v22
	v_add_f32_e32 v92, v92, v4
	ds_read_b128 v[4:7], v110 offset:48128
	v_add_f32_e32 v93, v93, v94
	v_add_f32_e32 v91, v91, v93
	s_waitcnt lgkmcnt(0)
	v_mul_f32_e32 v93, v5, v21
	v_mul_f32_e32 v5, v5, v53
	v_fmac_f32_e32 v93, v4, v20
	v_fmac_f32_e32 v5, v4, v52
	v_mul_f32_e32 v4, v7, v51
	v_fmac_f32_e32 v4, v6, v50
	v_mul_f32_e32 v94, v7, v19
	v_add_f32_e32 v4, v5, v4
	v_fmac_f32_e32 v94, v6, v18
	v_add_f32_e32 v92, v92, v4
	ds_read_b128 v[4:7], v110 offset:49152
	v_add_f32_e32 v93, v93, v94
	v_add_f32_e32 v91, v91, v93
	s_waitcnt lgkmcnt(0)
	v_mul_f32_e32 v93, v5, v49
	v_mul_f32_e32 v5, v5, v73
	v_fmac_f32_e32 v93, v4, v48
	v_fmac_f32_e32 v5, v4, v72
	v_mul_f32_e32 v4, v7, v71
	v_mul_f32_e32 v94, v7, v47
	v_fmac_f32_e32 v4, v6, v70
	v_fmac_f32_e32 v94, v6, v46
	v_add_f32_e32 v4, v5, v4
	v_add_f32_e32 v93, v93, v94
	v_add_f32_e32 v94, 0, v4
	ds_read_b128 v[4:7], v110 offset:50176
	v_add_f32_e32 v93, 0, v93
	s_waitcnt lgkmcnt(0)
	v_mul_f32_e32 v95, v5, v45
	v_mul_f32_e32 v5, v5, v81
	v_fmac_f32_e32 v95, v4, v44
	v_fmac_f32_e32 v5, v4, v80
	v_mul_f32_e32 v4, v7, v79
	v_fmac_f32_e32 v4, v6, v78
	v_mul_f32_e32 v96, v7, v43
	v_add_f32_e32 v4, v5, v4
	v_fmac_f32_e32 v96, v6, v42
	v_add_f32_e32 v94, v94, v4
	ds_read_b128 v[4:7], v110 offset:51200
	v_add_f32_e32 v95, v95, v96
	v_add_f32_e32 v93, v93, v95
	s_waitcnt lgkmcnt(0)
	v_mul_f32_e32 v95, v5, v41
	v_mul_f32_e32 v5, v5, v77
	v_fmac_f32_e32 v95, v4, v40
	v_fmac_f32_e32 v5, v4, v76
	v_mul_f32_e32 v4, v7, v75
	v_fmac_f32_e32 v4, v6, v74
	v_mul_f32_e32 v96, v7, v39
	v_add_f32_e32 v4, v5, v4
	v_fmac_f32_e32 v96, v6, v38
	v_add_f32_e32 v94, v94, v4
	ds_read_b128 v[4:7], v110 offset:52224
	v_add_f32_e32 v95, v95, v96
	v_add_f32_e32 v93, v93, v95
	s_waitcnt lgkmcnt(0)
	v_mul_f32_e32 v95, v5, v33
	v_mul_f32_e32 v5, v5, v65
	v_fmac_f32_e32 v95, v4, v32
	v_fmac_f32_e32 v5, v4, v64
	v_mul_f32_e32 v4, v7, v63
	v_fmac_f32_e32 v4, v6, v62
	v_mul_f32_e32 v96, v7, v31
	v_add_f32_e32 v4, v5, v4
	v_fmac_f32_e32 v96, v6, v30
	v_add_f32_e32 v94, v94, v4
	ds_read_b128 v[4:7], v110 offset:53248
	v_add_f32_e32 v95, v95, v96
	v_add_f32_e32 v93, v93, v95
	s_waitcnt lgkmcnt(0)
	v_mul_f32_e32 v95, v5, v37
	v_mul_f32_e32 v5, v5, v69
	v_fmac_f32_e32 v95, v4, v36
	v_fmac_f32_e32 v5, v4, v68
	v_mul_f32_e32 v4, v7, v67
	v_fmac_f32_e32 v4, v6, v66
	v_mul_f32_e32 v96, v7, v35
	v_add_f32_e32 v4, v5, v4
	v_fmac_f32_e32 v96, v6, v34
	v_add_f32_e32 v94, v94, v4
	ds_read_b128 v[4:7], v110 offset:54272
	v_add_f32_e32 v95, v95, v96
	v_add_f32_e32 v93, v93, v95
	s_waitcnt lgkmcnt(0)
	v_mul_f32_e32 v95, v5, v29
	v_mul_f32_e32 v5, v5, v61
	v_fmac_f32_e32 v95, v4, v28
	v_fmac_f32_e32 v5, v4, v60
	v_mul_f32_e32 v4, v7, v59
	v_fmac_f32_e32 v4, v6, v58
	v_mul_f32_e32 v96, v7, v27
	v_add_f32_e32 v4, v5, v4
	v_fmac_f32_e32 v96, v6, v26
	v_add_f32_e32 v94, v94, v4
	ds_read_b128 v[4:7], v110 offset:55296
	v_add_f32_e32 v95, v95, v96
	v_add_f32_e32 v93, v93, v95
	s_waitcnt lgkmcnt(0)
	v_mul_f32_e32 v95, v5, v25
	v_mul_f32_e32 v5, v5, v57
	v_fmac_f32_e32 v95, v4, v24
	v_fmac_f32_e32 v5, v4, v56
	v_mul_f32_e32 v4, v7, v55
	v_fmac_f32_e32 v4, v6, v54
	v_mul_f32_e32 v96, v7, v23
	v_add_f32_e32 v4, v5, v4
	v_fmac_f32_e32 v96, v6, v22
	v_add_f32_e32 v94, v94, v4
	ds_read_b128 v[4:7], v110 offset:56320
	v_add_f32_e32 v95, v95, v96
	v_add_f32_e32 v93, v93, v95
	s_waitcnt lgkmcnt(0)
	v_mul_f32_e32 v95, v5, v21
	v_mul_f32_e32 v5, v5, v53
	v_fmac_f32_e32 v95, v4, v20
	v_fmac_f32_e32 v5, v4, v52
	v_mul_f32_e32 v4, v7, v51
	v_fmac_f32_e32 v4, v6, v50
	v_mul_f32_e32 v96, v7, v19
	v_add_f32_e32 v4, v5, v4
	v_fmac_f32_e32 v96, v6, v18
	v_add_f32_e32 v94, v94, v4
	ds_read_b128 v[4:7], v110 offset:57344
	v_add_f32_e32 v95, v95, v96
	v_add_f32_e32 v93, v93, v95
	s_waitcnt lgkmcnt(0)
	v_mul_f32_e32 v95, v5, v49
	v_mul_f32_e32 v5, v5, v73
	v_fmac_f32_e32 v95, v4, v48
	v_fmac_f32_e32 v5, v4, v72
	v_mul_f32_e32 v4, v7, v71
	v_mul_f32_e32 v96, v7, v47
	v_fmac_f32_e32 v4, v6, v70
	v_fmac_f32_e32 v96, v6, v46
	v_add_f32_e32 v4, v5, v4
	v_add_f32_e32 v95, v95, v96
	v_add_f32_e32 v96, 0, v4
	ds_read_b128 v[4:7], v110 offset:58368
	v_add_f32_e32 v95, 0, v95
	s_waitcnt lgkmcnt(0)
	v_mul_f32_e32 v97, v5, v45
	v_mul_f32_e32 v5, v5, v81
	v_fmac_f32_e32 v97, v4, v44
	v_fmac_f32_e32 v5, v4, v80
	v_mul_f32_e32 v4, v7, v79
	v_fmac_f32_e32 v4, v6, v78
	v_mul_f32_e32 v98, v7, v43
	v_add_f32_e32 v4, v5, v4
	v_fmac_f32_e32 v98, v6, v42
	v_add_f32_e32 v96, v96, v4
	ds_read_b128 v[4:7], v110 offset:59392
	v_add_f32_e32 v97, v97, v98
	v_add_f32_e32 v95, v95, v97
	s_waitcnt lgkmcnt(0)
	v_mul_f32_e32 v97, v5, v41
	v_mul_f32_e32 v5, v5, v77
	v_fmac_f32_e32 v97, v4, v40
	v_fmac_f32_e32 v5, v4, v76
	v_mul_f32_e32 v4, v7, v75
	v_fmac_f32_e32 v4, v6, v74
	v_mul_f32_e32 v98, v7, v39
	v_add_f32_e32 v4, v5, v4
	v_fmac_f32_e32 v98, v6, v38
	v_add_f32_e32 v96, v96, v4
	ds_read_b128 v[4:7], v110 offset:60416
	v_add_f32_e32 v97, v97, v98
	v_add_f32_e32 v95, v95, v97
	s_waitcnt lgkmcnt(0)
	v_mul_f32_e32 v97, v5, v33
	v_mul_f32_e32 v5, v5, v65
	v_fmac_f32_e32 v97, v4, v32
	v_fmac_f32_e32 v5, v4, v64
	v_mul_f32_e32 v4, v7, v63
	v_fmac_f32_e32 v4, v6, v62
	v_mul_f32_e32 v98, v7, v31
	v_add_f32_e32 v4, v5, v4
	v_fmac_f32_e32 v98, v6, v30
	v_add_f32_e32 v96, v96, v4
	ds_read_b128 v[4:7], v110 offset:61440
	v_add_f32_e32 v97, v97, v98
	v_add_f32_e32 v95, v95, v97
	s_waitcnt lgkmcnt(0)
	v_mul_f32_e32 v97, v5, v37
	v_mul_f32_e32 v5, v5, v69
	v_fmac_f32_e32 v97, v4, v36
	v_fmac_f32_e32 v5, v4, v68
	v_mul_f32_e32 v4, v7, v67
	v_fmac_f32_e32 v4, v6, v66
	v_mul_f32_e32 v98, v7, v35
	v_add_f32_e32 v4, v5, v4
	v_fmac_f32_e32 v98, v6, v34
	v_add_f32_e32 v96, v96, v4
	ds_read_b128 v[4:7], v110 offset:62464
	v_add_f32_e32 v97, v97, v98
	v_add_f32_e32 v95, v95, v97
	s_waitcnt lgkmcnt(0)
	v_mul_f32_e32 v97, v5, v29
	v_mul_f32_e32 v5, v5, v61
	v_fmac_f32_e32 v97, v4, v28
	v_fmac_f32_e32 v5, v4, v60
	v_mul_f32_e32 v4, v7, v59
	v_fmac_f32_e32 v4, v6, v58
	v_mul_f32_e32 v98, v7, v27
	v_add_f32_e32 v4, v5, v4
	v_fmac_f32_e32 v98, v6, v26
	v_add_f32_e32 v96, v96, v4
	ds_read_b128 v[4:7], v110 offset:63488
	v_add_f32_e32 v97, v97, v98
	v_add_f32_e32 v95, v95, v97
	s_waitcnt lgkmcnt(0)
	v_mul_f32_e32 v97, v5, v25
	v_mul_f32_e32 v5, v5, v57
	v_fmac_f32_e32 v97, v4, v24
	v_fmac_f32_e32 v5, v4, v56
	v_mul_f32_e32 v4, v7, v55
	v_fmac_f32_e32 v4, v6, v54
	v_mul_f32_e32 v98, v7, v23
	v_add_f32_e32 v4, v5, v4
	v_fmac_f32_e32 v98, v6, v22
	v_add_f32_e32 v96, v96, v4
	ds_read_b128 v[4:7], v110 offset:64512
	v_add_f32_e32 v97, v97, v98
	v_add_f32_e32 v95, v95, v97
	s_waitcnt lgkmcnt(0)
	v_mul_f32_e32 v97, v5, v21
	v_mul_f32_e32 v5, v5, v53
	v_fmac_f32_e32 v97, v4, v20
	v_fmac_f32_e32 v5, v4, v52
	v_mul_f32_e32 v4, v7, v51
	v_fmac_f32_e32 v4, v6, v50
	v_mul_f32_e32 v98, v7, v19
	v_add_f32_e32 v4, v5, v4
	v_fmac_f32_e32 v98, v6, v18
	v_add_f32_e32 v96, v96, v4
	ds_read_b128 v[4:7], v117
	v_add_f32_e32 v97, v97, v98
	v_add_f32_e32 v95, v95, v97
	s_waitcnt lgkmcnt(0)
	v_mul_f32_e32 v97, v5, v49
	v_mul_f32_e32 v5, v5, v73
	v_fmac_f32_e32 v97, v4, v48
	v_fmac_f32_e32 v5, v4, v72
	v_mul_f32_e32 v4, v7, v71
	v_mul_f32_e32 v98, v7, v47
	v_fmac_f32_e32 v4, v6, v70
	v_fmac_f32_e32 v98, v6, v46
	v_add_f32_e32 v4, v5, v4
	v_add_f32_e32 v97, v97, v98
	v_add_f32_e32 v98, 0, v4
	ds_read_b128 v[4:7], v118
	v_add_f32_e32 v97, 0, v97
	s_waitcnt lgkmcnt(0)
	v_mul_f32_e32 v99, v5, v45
	v_mul_f32_e32 v5, v5, v81
	v_fmac_f32_e32 v99, v4, v44
	v_fmac_f32_e32 v5, v4, v80
	v_mul_f32_e32 v4, v7, v79
	v_fmac_f32_e32 v4, v6, v78
	v_mul_f32_e32 v100, v7, v43
	v_add_f32_e32 v4, v5, v4
	v_fmac_f32_e32 v100, v6, v42
	v_add_f32_e32 v98, v98, v4
	ds_read_b128 v[4:7], v119
	v_add_f32_e32 v99, v99, v100
	v_add_f32_e32 v97, v97, v99
	s_waitcnt lgkmcnt(0)
	v_mul_f32_e32 v99, v5, v41
	v_mul_f32_e32 v5, v5, v77
	v_fmac_f32_e32 v99, v4, v40
	v_fmac_f32_e32 v5, v4, v76
	v_mul_f32_e32 v4, v7, v75
	v_fmac_f32_e32 v4, v6, v74
	v_mul_f32_e32 v100, v7, v39
	v_add_f32_e32 v4, v5, v4
	v_fmac_f32_e32 v100, v6, v38
	v_add_f32_e32 v98, v98, v4
	ds_read_b128 v[4:7], v120
	v_add_f32_e32 v99, v99, v100
	v_add_f32_e32 v97, v97, v99
	s_waitcnt lgkmcnt(0)
	v_mul_f32_e32 v99, v5, v33
	v_mul_f32_e32 v5, v5, v65
	v_fmac_f32_e32 v99, v4, v32
	v_mul_f32_e32 v100, v7, v31
	v_fmac_f32_e32 v5, v4, v64
	v_mul_f32_e32 v4, v7, v63
	v_fmac_f32_e32 v100, v6, v30
	v_fmac_f32_e32 v4, v6, v62
	v_add_f32_e32 v99, v99, v100
	v_add_f32_e32 v4, v5, v4
	v_add_f32_e32 v97, v97, v99
	v_add_f32_e32 v99, v98, v4
	ds_read_b128 v[4:7], v121
	s_waitcnt lgkmcnt(0)
	v_mul_f32_e32 v98, v5, v37
	v_mul_f32_e32 v5, v5, v69
	v_fmac_f32_e32 v98, v4, v36
	v_mul_f32_e32 v100, v7, v35
	v_fmac_f32_e32 v5, v4, v68
	v_mul_f32_e32 v4, v7, v67
	v_fmac_f32_e32 v100, v6, v34
	v_fmac_f32_e32 v4, v6, v66
	v_add_f32_e32 v98, v98, v100
	v_add_f32_e32 v4, v5, v4
	v_add_f32_e32 v98, v97, v98
	v_add_f32_e32 v97, v99, v4
	ds_read_b128 v[4:7], v122
	s_waitcnt lgkmcnt(0)
	v_mul_f32_e32 v99, v5, v29
	v_mul_f32_e32 v5, v5, v61
	v_fmac_f32_e32 v99, v4, v28
	v_fmac_f32_e32 v5, v4, v60
	v_mul_f32_e32 v4, v7, v59
	v_fmac_f32_e32 v4, v6, v58
	v_mul_f32_e32 v100, v7, v27
	v_add_f32_e32 v4, v5, v4
	v_fmac_f32_e32 v100, v6, v26
	v_add_f32_e32 v97, v97, v4
	ds_read_b128 v[4:7], v123
	v_add_f32_e32 v99, v99, v100
	v_add_f32_e32 v98, v98, v99
	s_waitcnt lgkmcnt(0)
	v_mul_f32_e32 v99, v5, v25
	v_mul_f32_e32 v100, v7, v23
	v_fmac_f32_e32 v99, v4, v24
	v_fmac_f32_e32 v100, v6, v22
	v_add_f32_e32 v99, v99, v100
	v_add_f32_e32 v102, v98, v99
	ds_read_b128 v[98:101], v124
	v_mul_f32_e32 v5, v5, v57
	v_fmac_f32_e32 v5, v4, v56
	v_mul_f32_e32 v4, v7, v55
	v_fmac_f32_e32 v4, v6, v54
	v_add_f32_e32 v4, v5, v4
	v_add_f32_e32 v5, v97, v4
	s_waitcnt lgkmcnt(0)
	v_mul_f32_e32 v4, v99, v21
	v_mul_f32_e32 v6, v101, v19
	v_fmac_f32_e32 v4, v98, v20
	v_fmac_f32_e32 v6, v100, v18
	v_add_f32_e32 v4, v4, v6
	v_mul_f32_e32 v6, v99, v53
	v_mul_f32_e32 v7, v101, v51
	v_fmac_f32_e32 v6, v98, v52
	v_fmac_f32_e32 v7, v100, v50
	ds_read_b128 v[98:101], v125
	v_add_f32_e32 v6, v6, v7
	v_add_f32_e32 v5, v5, v6
	v_add_f32_e32 v4, v102, v4
	s_waitcnt lgkmcnt(0)
	v_mul_f32_e32 v6, v99, v49
	v_mul_f32_e32 v7, v101, v47
	v_fmac_f32_e32 v6, v98, v48
	v_fmac_f32_e32 v7, v100, v46
	v_add_f32_e32 v6, v6, v7
	v_mul_f32_e32 v7, v99, v73
	v_mul_f32_e32 v97, v101, v71
	v_fmac_f32_e32 v7, v98, v72
	v_fmac_f32_e32 v97, v100, v70
	ds_read_b128 v[98:101], v126
	v_add_f32_e32 v7, v7, v97
	v_add_f32_e32 v6, 0, v6
	v_add_f32_e32 v7, 0, v7
	s_waitcnt lgkmcnt(0)
	v_mul_f32_e32 v97, v99, v45
	v_mul_f32_e32 v102, v101, v43
	v_fmac_f32_e32 v97, v98, v44
	v_fmac_f32_e32 v102, v100, v42
	v_add_f32_e32 v97, v97, v102
	v_add_f32_e32 v6, v6, v97
	v_mul_f32_e32 v97, v99, v81
	v_fmac_f32_e32 v97, v98, v80
	v_mul_f32_e32 v98, v101, v79
	v_fmac_f32_e32 v98, v100, v78
	v_add_f32_e32 v97, v97, v98
	ds_read_b128 v[98:101], v127
	v_add_f32_e32 v7, v7, v97
	s_waitcnt lgkmcnt(0)
	v_mul_f32_e32 v97, v99, v41
	v_mul_f32_e32 v102, v101, v39
	v_fmac_f32_e32 v97, v98, v40
	v_fmac_f32_e32 v102, v100, v38
	v_add_f32_e32 v97, v97, v102
	v_add_f32_e32 v6, v6, v97
	v_mul_f32_e32 v97, v99, v77
	v_fmac_f32_e32 v97, v98, v76
	v_mul_f32_e32 v98, v101, v75
	v_fmac_f32_e32 v98, v100, v74
	v_add_f32_e32 v97, v97, v98
	ds_read_b128 v[98:101], v128
	v_add_f32_e32 v7, v7, v97
	s_waitcnt lgkmcnt(0)
	v_mul_f32_e32 v97, v99, v33
	v_mul_f32_e32 v102, v101, v31
	v_fmac_f32_e32 v97, v98, v32
	v_fmac_f32_e32 v102, v100, v30
	v_add_f32_e32 v97, v97, v102
	v_add_f32_e32 v6, v6, v97
	v_mul_f32_e32 v97, v99, v65
	v_fmac_f32_e32 v97, v98, v64
	v_mul_f32_e32 v98, v101, v63
	v_fmac_f32_e32 v98, v100, v62
	v_add_f32_e32 v97, v97, v98
	ds_read_b128 v[98:101], v129
	v_add_f32_e32 v7, v7, v97
	s_waitcnt lgkmcnt(0)
	v_mul_f32_e32 v97, v99, v37
	v_mul_f32_e32 v102, v101, v35
	v_fmac_f32_e32 v97, v98, v36
	v_fmac_f32_e32 v102, v100, v34
	v_add_f32_e32 v97, v97, v102
	v_add_f32_e32 v6, v6, v97
	v_mul_f32_e32 v97, v99, v69
	v_fmac_f32_e32 v97, v98, v68
	v_mul_f32_e32 v98, v101, v67
	v_fmac_f32_e32 v98, v100, v66
	v_add_f32_e32 v97, v97, v98
	ds_read_b128 v[98:101], v130
	v_add_f32_e32 v7, v7, v97
	s_waitcnt lgkmcnt(0)
	v_mul_f32_e32 v97, v99, v29
	v_mul_f32_e32 v102, v101, v27
	v_fmac_f32_e32 v97, v98, v28
	v_fmac_f32_e32 v102, v100, v26
	v_add_f32_e32 v97, v97, v102
	v_add_f32_e32 v6, v6, v97
	v_mul_f32_e32 v97, v99, v61
	v_fmac_f32_e32 v97, v98, v60
	v_mul_f32_e32 v98, v101, v59
	v_fmac_f32_e32 v98, v100, v58
	v_add_f32_e32 v97, v97, v98
	ds_read_b128 v[98:101], v131
	v_add_f32_e32 v7, v7, v97
	s_waitcnt lgkmcnt(0)
	v_mul_f32_e32 v97, v99, v25
	v_mul_f32_e32 v102, v101, v23
	v_fmac_f32_e32 v97, v98, v24
	v_fmac_f32_e32 v102, v100, v22
	v_add_f32_e32 v97, v97, v102
	v_add_f32_e32 v6, v6, v97
	v_mul_f32_e32 v97, v99, v57
	v_fmac_f32_e32 v97, v98, v56
	v_mul_f32_e32 v98, v101, v55
	v_fmac_f32_e32 v98, v100, v54
	v_add_f32_e32 v97, v97, v98
	ds_read_b128 v[98:101], v132
	v_add_f32_e32 v7, v7, v97
	s_waitcnt lgkmcnt(0)
	v_mul_f32_e32 v97, v99, v21
	v_mul_f32_e32 v102, v101, v19
	v_fmac_f32_e32 v97, v98, v20
	v_fmac_f32_e32 v102, v100, v18
	v_add_f32_e32 v97, v97, v102
	v_add_f32_e32 v6, v6, v97
	v_mul_f32_e32 v97, v99, v53
	v_fmac_f32_e32 v97, v98, v52
	v_mul_f32_e32 v98, v101, v51
	v_fmac_f32_e32 v98, v100, v50
	v_add_f32_e32 v97, v97, v98
	ds_read_b128 v[98:101], v133
	v_add_f32_e32 v7, v7, v97
	s_waitcnt lgkmcnt(0)
	v_mul_f32_e32 v97, v99, v49
	v_mul_f32_e32 v99, v99, v73
	v_fmac_f32_e32 v97, v98, v48
	v_fmac_f32_e32 v99, v98, v72
	v_mul_f32_e32 v98, v101, v71
	v_mul_f32_e32 v102, v101, v47
	v_fmac_f32_e32 v98, v100, v70
	v_fmac_f32_e32 v102, v100, v46
	v_add_f32_e32 v98, v99, v98
	v_add_f32_e32 v97, v97, v102
	v_add_f32_e32 v102, 0, v98
	ds_read_b128 v[98:101], v134
	v_add_f32_e32 v97, 0, v97
	s_waitcnt lgkmcnt(0)
	v_mul_f32_e32 v103, v99, v45
	v_mul_f32_e32 v99, v99, v81
	v_fmac_f32_e32 v103, v98, v44
	v_fmac_f32_e32 v99, v98, v80
	v_mul_f32_e32 v98, v101, v79
	v_fmac_f32_e32 v98, v100, v78
	v_mul_f32_e32 v104, v101, v43
	v_add_f32_e32 v98, v99, v98
	v_fmac_f32_e32 v104, v100, v42
	v_add_f32_e32 v102, v102, v98
	ds_read_b128 v[98:101], v135
	v_add_f32_e32 v103, v103, v104
	v_add_f32_e32 v97, v97, v103
	s_waitcnt lgkmcnt(0)
	v_mul_f32_e32 v103, v99, v41
	v_mul_f32_e32 v99, v99, v77
	v_fmac_f32_e32 v103, v98, v40
	v_fmac_f32_e32 v99, v98, v76
	v_mul_f32_e32 v98, v101, v75
	v_fmac_f32_e32 v98, v100, v74
	v_mul_f32_e32 v104, v101, v39
	v_add_f32_e32 v98, v99, v98
	v_fmac_f32_e32 v104, v100, v38
	v_add_f32_e32 v102, v102, v98
	ds_read_b128 v[98:101], v136
	v_add_f32_e32 v103, v103, v104
	v_add_f32_e32 v97, v97, v103
	s_waitcnt lgkmcnt(0)
	v_mul_f32_e32 v103, v99, v33
	v_mul_f32_e32 v99, v99, v65
	v_fmac_f32_e32 v103, v98, v32
	v_fmac_f32_e32 v99, v98, v64
	v_mul_f32_e32 v98, v101, v63
	v_fmac_f32_e32 v98, v100, v62
	v_mul_f32_e32 v104, v101, v31
	v_add_f32_e32 v98, v99, v98
	v_fmac_f32_e32 v104, v100, v30
	v_add_f32_e32 v102, v102, v98
	ds_read_b128 v[98:101], v137
	v_add_f32_e32 v103, v103, v104
	v_add_f32_e32 v97, v97, v103
	s_waitcnt lgkmcnt(0)
	v_mul_f32_e32 v103, v99, v37
	v_mul_f32_e32 v99, v99, v69
	v_fmac_f32_e32 v103, v98, v36
	v_fmac_f32_e32 v99, v98, v68
	v_mul_f32_e32 v98, v101, v67
	v_fmac_f32_e32 v98, v100, v66
	v_mul_f32_e32 v104, v101, v35
	v_add_f32_e32 v98, v99, v98
	v_fmac_f32_e32 v104, v100, v34
	v_add_f32_e32 v102, v102, v98
	ds_read_b128 v[98:101], v138
	v_add_f32_e32 v103, v103, v104
	v_add_f32_e32 v97, v97, v103
	s_waitcnt lgkmcnt(0)
	v_mul_f32_e32 v103, v99, v29
	v_mul_f32_e32 v99, v99, v61
	v_fmac_f32_e32 v103, v98, v28
	v_fmac_f32_e32 v99, v98, v60
	v_mul_f32_e32 v98, v101, v59
	v_fmac_f32_e32 v98, v100, v58
	v_mul_f32_e32 v104, v101, v27
	v_add_f32_e32 v98, v99, v98
	v_fmac_f32_e32 v104, v100, v26
	v_add_f32_e32 v102, v102, v98
	ds_read_b128 v[98:101], v139
	v_add_f32_e32 v103, v103, v104
	v_add_f32_e32 v97, v97, v103
	s_waitcnt lgkmcnt(0)
	v_mul_f32_e32 v103, v99, v25
	v_mul_f32_e32 v99, v99, v57
	v_fmac_f32_e32 v103, v98, v24
	v_fmac_f32_e32 v99, v98, v56
	v_mul_f32_e32 v98, v101, v55
	v_fmac_f32_e32 v98, v100, v54
	v_mul_f32_e32 v104, v101, v23
	v_add_f32_e32 v98, v99, v98
	v_fmac_f32_e32 v104, v100, v22
	v_add_f32_e32 v102, v102, v98
	ds_read_b128 v[98:101], v140
	v_add_f32_e32 v103, v103, v104
	v_add_f32_e32 v97, v97, v103
	s_waitcnt lgkmcnt(0)
	v_mul_f32_e32 v103, v99, v21
	v_mul_f32_e32 v99, v99, v53
	v_fmac_f32_e32 v103, v98, v20
	v_mul_f32_e32 v104, v101, v19
	v_fmac_f32_e32 v99, v98, v52
	v_mul_f32_e32 v98, v101, v51
	v_fmac_f32_e32 v104, v100, v18
	v_fmac_f32_e32 v98, v100, v50
	v_add_f32_e32 v103, v103, v104
	v_add_f32_e32 v98, v99, v98
	v_add_f32_e32 v97, v97, v103
	v_add_f32_e32 v98, v102, v98
	ds_read_b128 v[100:103], v141
	s_waitcnt lgkmcnt(0)
	v_mul_f32_e32 v99, v101, v49
	v_mul_f32_e32 v101, v101, v73
	v_fmac_f32_e32 v99, v100, v48
	v_fmac_f32_e32 v101, v100, v72
	v_mul_f32_e32 v100, v103, v71
	v_mul_f32_e32 v104, v103, v47
	v_fmac_f32_e32 v100, v102, v70
	v_fmac_f32_e32 v104, v102, v46
	v_add_f32_e32 v100, v101, v100
	v_add_f32_e32 v99, v99, v104
	v_add_f32_e32 v104, 0, v100
	ds_read_b128 v[100:103], v142
	v_add_f32_e32 v99, 0, v99
	s_waitcnt lgkmcnt(0)
	v_mul_f32_e32 v105, v101, v45
	v_mul_f32_e32 v101, v101, v81
	v_fmac_f32_e32 v105, v100, v44
	v_fmac_f32_e32 v101, v100, v80
	v_mul_f32_e32 v100, v103, v79
	v_fmac_f32_e32 v100, v102, v78
	v_mul_f32_e32 v106, v103, v43
	v_add_f32_e32 v100, v101, v100
	v_fmac_f32_e32 v106, v102, v42
	v_add_f32_e32 v104, v104, v100
	ds_read_b128 v[100:103], v143
	v_add_f32_e32 v105, v105, v106
	v_add_f32_e32 v99, v99, v105
	s_waitcnt lgkmcnt(0)
	v_mul_f32_e32 v105, v101, v41
	v_mul_f32_e32 v101, v101, v77
	v_fmac_f32_e32 v105, v100, v40
	v_fmac_f32_e32 v101, v100, v76
	v_mul_f32_e32 v100, v103, v75
	v_fmac_f32_e32 v100, v102, v74
	v_mul_f32_e32 v106, v103, v39
	v_add_f32_e32 v100, v101, v100
	v_fmac_f32_e32 v106, v102, v38
	v_add_f32_e32 v104, v104, v100
	ds_read_b128 v[100:103], v144
	v_add_f32_e32 v105, v105, v106
	v_add_f32_e32 v99, v99, v105
	s_waitcnt lgkmcnt(0)
	v_mul_f32_e32 v105, v101, v33
	v_mul_f32_e32 v101, v101, v65
	v_fmac_f32_e32 v105, v100, v32
	v_fmac_f32_e32 v101, v100, v64
	v_mul_f32_e32 v100, v103, v63
	v_fmac_f32_e32 v100, v102, v62
	v_mul_f32_e32 v106, v103, v31
	v_add_f32_e32 v100, v101, v100
	v_fmac_f32_e32 v106, v102, v30
	v_add_f32_e32 v104, v104, v100
	ds_read_b128 v[100:103], v145
	v_add_f32_e32 v105, v105, v106
	v_add_f32_e32 v99, v99, v105
	s_waitcnt lgkmcnt(0)
	v_mul_f32_e32 v105, v101, v37
	v_mul_f32_e32 v101, v101, v69
	v_fmac_f32_e32 v105, v100, v36
	v_fmac_f32_e32 v101, v100, v68
	v_mul_f32_e32 v100, v103, v67
	v_fmac_f32_e32 v100, v102, v66
	v_mul_f32_e32 v106, v103, v35
	v_add_f32_e32 v100, v101, v100
	v_fmac_f32_e32 v106, v102, v34
	v_add_f32_e32 v104, v104, v100
	ds_read_b128 v[100:103], v146
	v_add_f32_e32 v105, v105, v106
	v_add_f32_e32 v99, v99, v105
	s_waitcnt lgkmcnt(0)
	v_mul_f32_e32 v105, v101, v29
	v_mul_f32_e32 v101, v101, v61
	v_fmac_f32_e32 v105, v100, v28
	v_fmac_f32_e32 v101, v100, v60
	v_mul_f32_e32 v100, v103, v59
	v_fmac_f32_e32 v100, v102, v58
	v_mul_f32_e32 v106, v103, v27
	v_add_f32_e32 v100, v101, v100
	v_fmac_f32_e32 v106, v102, v26
	v_add_f32_e32 v104, v104, v100
	ds_read_b128 v[100:103], v147
	v_add_f32_e32 v105, v105, v106
	v_add_f32_e32 v99, v99, v105
	s_waitcnt lgkmcnt(0)
	v_mul_f32_e32 v105, v101, v25
	v_mul_f32_e32 v101, v101, v57
	v_fmac_f32_e32 v105, v100, v24
	v_fmac_f32_e32 v101, v100, v56
	v_mul_f32_e32 v100, v103, v55
	v_fmac_f32_e32 v100, v102, v54
	v_mul_f32_e32 v106, v103, v23
	v_add_f32_e32 v100, v101, v100
	v_fmac_f32_e32 v106, v102, v22
	v_add_f32_e32 v104, v104, v100
	ds_read_b128 v[100:103], v148
	v_add_f32_e32 v105, v105, v106
	v_add_f32_e32 v99, v99, v105
	s_waitcnt lgkmcnt(0)
	v_mul_f32_e32 v105, v101, v21
	v_mul_f32_e32 v101, v101, v53
	v_fmac_f32_e32 v105, v100, v20
	v_mul_f32_e32 v106, v103, v19
	v_fmac_f32_e32 v101, v100, v52
	v_mul_f32_e32 v100, v103, v51
	v_fmac_f32_e32 v106, v102, v18
	v_fmac_f32_e32 v100, v102, v50
	v_add_f32_e32 v105, v105, v106
	v_add_f32_e32 v100, v101, v100
	v_add_f32_e32 v99, v99, v105
	v_add_f32_e32 v100, v104, v100
	ds_read_b128 v[102:105], v149
	s_waitcnt lgkmcnt(0)
	v_mul_f32_e32 v101, v103, v49
	v_mul_f32_e32 v103, v103, v73
	v_fmac_f32_e32 v101, v102, v48
	v_fmac_f32_e32 v103, v102, v72
	v_mul_f32_e32 v102, v105, v71
	v_mul_f32_e32 v106, v105, v47
	v_fmac_f32_e32 v102, v104, v70
	v_fmac_f32_e32 v106, v104, v46
	v_add_f32_e32 v102, v103, v102
	v_add_f32_e32 v101, v101, v106
	v_add_f32_e32 v106, 0, v102
	ds_read_b128 v[102:105], v150
	v_add_f32_e32 v101, 0, v101
	s_waitcnt lgkmcnt(0)
	v_mul_f32_e32 v107, v103, v45
	v_mul_f32_e32 v103, v103, v81
	v_fmac_f32_e32 v107, v102, v44
	v_fmac_f32_e32 v103, v102, v80
	v_mul_f32_e32 v102, v105, v79
	v_fmac_f32_e32 v102, v104, v78
	v_mul_f32_e32 v108, v105, v43
	v_add_f32_e32 v102, v103, v102
	v_fmac_f32_e32 v108, v104, v42
	v_add_f32_e32 v106, v106, v102
	ds_read_b128 v[102:105], v151
	v_add_f32_e32 v107, v107, v108
	v_add_f32_e32 v101, v101, v107
	s_waitcnt lgkmcnt(0)
	v_mul_f32_e32 v107, v103, v41
	v_mul_f32_e32 v103, v103, v77
	v_fmac_f32_e32 v107, v102, v40
	v_fmac_f32_e32 v103, v102, v76
	v_mul_f32_e32 v102, v105, v75
	v_fmac_f32_e32 v102, v104, v74
	v_mul_f32_e32 v108, v105, v39
	v_add_f32_e32 v102, v103, v102
	v_fmac_f32_e32 v108, v104, v38
	v_add_f32_e32 v106, v106, v102
	ds_read_b128 v[102:105], v152
	v_add_f32_e32 v107, v107, v108
	v_add_f32_e32 v101, v101, v107
	s_waitcnt lgkmcnt(0)
	v_mul_f32_e32 v107, v103, v33
	v_mul_f32_e32 v103, v103, v65
	v_fmac_f32_e32 v107, v102, v32
	v_fmac_f32_e32 v103, v102, v64
	v_mul_f32_e32 v102, v105, v63
	v_fmac_f32_e32 v102, v104, v62
	v_mul_f32_e32 v108, v105, v31
	v_add_f32_e32 v102, v103, v102
	v_fmac_f32_e32 v108, v104, v30
	v_add_f32_e32 v106, v106, v102
	ds_read_b128 v[102:105], v153
	v_add_f32_e32 v107, v107, v108
	v_add_f32_e32 v101, v101, v107
	s_waitcnt lgkmcnt(0)
	v_mul_f32_e32 v107, v103, v37
	v_mul_f32_e32 v103, v103, v69
	v_fmac_f32_e32 v107, v102, v36
	v_fmac_f32_e32 v103, v102, v68
	v_mul_f32_e32 v102, v105, v67
	v_fmac_f32_e32 v102, v104, v66
	v_mul_f32_e32 v108, v105, v35
	v_add_f32_e32 v102, v103, v102
	v_fmac_f32_e32 v108, v104, v34
	v_add_f32_e32 v106, v106, v102
	ds_read_b128 v[102:105], v154
	v_add_f32_e32 v107, v107, v108
	v_add_f32_e32 v101, v101, v107
	s_waitcnt lgkmcnt(0)
	v_mul_f32_e32 v107, v103, v29
	v_mul_f32_e32 v103, v103, v61
	v_fmac_f32_e32 v107, v102, v28
	v_fmac_f32_e32 v103, v102, v60
	v_mul_f32_e32 v102, v105, v59
	v_fmac_f32_e32 v102, v104, v58
	v_mul_f32_e32 v108, v105, v27
	v_add_f32_e32 v102, v103, v102
	v_fmac_f32_e32 v108, v104, v26
	v_add_f32_e32 v106, v106, v102
	ds_read_b128 v[102:105], v155
	v_add_f32_e32 v107, v107, v108
	v_add_f32_e32 v101, v101, v107
	s_waitcnt lgkmcnt(0)
	v_mul_f32_e32 v107, v103, v25
	v_mul_f32_e32 v103, v103, v57
	v_fmac_f32_e32 v107, v102, v24
	v_fmac_f32_e32 v103, v102, v56
	v_mul_f32_e32 v102, v105, v55
	v_fmac_f32_e32 v102, v104, v54
	v_mul_f32_e32 v108, v105, v23
	v_add_f32_e32 v102, v103, v102
	v_fmac_f32_e32 v108, v104, v22
	v_add_f32_e32 v106, v106, v102
	ds_read_b128 v[102:105], v156
	v_add_f32_e32 v107, v107, v108
	v_add_f32_e32 v101, v101, v107
	s_waitcnt lgkmcnt(0)
	v_mul_f32_e32 v107, v103, v21
	v_mul_f32_e32 v103, v103, v53
	v_fmac_f32_e32 v107, v102, v20
	v_mul_f32_e32 v108, v105, v19
	v_fmac_f32_e32 v103, v102, v52
	v_mul_f32_e32 v102, v105, v51
	v_fmac_f32_e32 v108, v104, v18
	v_fmac_f32_e32 v102, v104, v50
	v_add_f32_e32 v107, v107, v108
	v_add_f32_e32 v102, v103, v102
	v_add_f32_e32 v101, v101, v107
	v_add_f32_e32 v102, v106, v102
	ds_read_b128 v[104:107], v157
	s_waitcnt lgkmcnt(0)
	v_mul_f32_e32 v103, v105, v49
	v_mul_f32_e32 v105, v105, v73
	v_fmac_f32_e32 v103, v104, v48
	v_fmac_f32_e32 v105, v104, v72
	v_mul_f32_e32 v104, v107, v71
	v_mul_f32_e32 v108, v107, v47
	v_fmac_f32_e32 v104, v106, v70
	v_fmac_f32_e32 v108, v106, v46
	v_add_f32_e32 v104, v105, v104
	v_add_f32_e32 v103, v103, v108
	v_add_f32_e32 v108, 0, v104
	ds_read_b128 v[104:107], v158
	v_add_f32_e32 v103, 0, v103
	s_waitcnt lgkmcnt(0)
	v_mul_f32_e32 v109, v105, v45
	v_mul_f32_e32 v105, v105, v81
	v_fmac_f32_e32 v109, v104, v44
	v_fmac_f32_e32 v105, v104, v80
	v_mul_f32_e32 v104, v107, v79
	v_fmac_f32_e32 v104, v106, v78
	v_mul_f32_e32 v191, v107, v43
	v_add_f32_e32 v104, v105, v104
	v_fmac_f32_e32 v191, v106, v42
	v_add_f32_e32 v108, v108, v104
	ds_read_b128 v[104:107], v159
	v_add_f32_e32 v109, v109, v191
	v_add_f32_e32 v103, v103, v109
	s_waitcnt lgkmcnt(0)
	v_mul_f32_e32 v109, v105, v41
	v_mul_f32_e32 v105, v105, v77
	v_fmac_f32_e32 v109, v104, v40
	v_fmac_f32_e32 v105, v104, v76
	v_mul_f32_e32 v104, v107, v75
	v_fmac_f32_e32 v104, v106, v74
	v_mul_f32_e32 v191, v107, v39
	v_add_f32_e32 v104, v105, v104
	v_fmac_f32_e32 v191, v106, v38
	v_add_f32_e32 v108, v108, v104
	ds_read_b128 v[104:107], v160
	v_add_f32_e32 v109, v109, v191
	v_add_f32_e32 v103, v103, v109
	s_waitcnt lgkmcnt(0)
	v_mul_f32_e32 v109, v105, v33
	v_mul_f32_e32 v105, v105, v65
	v_fmac_f32_e32 v109, v104, v32
	v_fmac_f32_e32 v105, v104, v64
	v_mul_f32_e32 v104, v107, v63
	v_fmac_f32_e32 v104, v106, v62
	v_mul_f32_e32 v191, v107, v31
	v_add_f32_e32 v104, v105, v104
	v_fmac_f32_e32 v191, v106, v30
	v_add_f32_e32 v108, v108, v104
	ds_read_b128 v[104:107], v161
	v_add_f32_e32 v109, v109, v191
	v_add_f32_e32 v103, v103, v109
	s_waitcnt lgkmcnt(0)
	v_mul_f32_e32 v109, v105, v37
	v_mul_f32_e32 v105, v105, v69
	v_fmac_f32_e32 v109, v104, v36
	v_fmac_f32_e32 v105, v104, v68
	v_mul_f32_e32 v104, v107, v67
	v_fmac_f32_e32 v104, v106, v66
	v_mul_f32_e32 v191, v107, v35
	v_add_f32_e32 v104, v105, v104
	v_fmac_f32_e32 v191, v106, v34
	v_add_f32_e32 v108, v108, v104
	ds_read_b128 v[104:107], v162
	v_add_f32_e32 v109, v109, v191
	v_add_f32_e32 v103, v103, v109
	s_waitcnt lgkmcnt(0)
	v_mul_f32_e32 v109, v105, v29
	v_mul_f32_e32 v105, v105, v61
	v_fmac_f32_e32 v109, v104, v28
	v_fmac_f32_e32 v105, v104, v60
	v_mul_f32_e32 v104, v107, v59
	v_fmac_f32_e32 v104, v106, v58
	v_mul_f32_e32 v191, v107, v27
	v_add_f32_e32 v104, v105, v104
	v_fmac_f32_e32 v191, v106, v26
	v_add_f32_e32 v108, v108, v104
	ds_read_b128 v[104:107], v163
	v_add_f32_e32 v109, v109, v191
	v_add_f32_e32 v103, v103, v109
	s_waitcnt lgkmcnt(0)
	v_mul_f32_e32 v109, v105, v25
	v_mul_f32_e32 v105, v105, v57
	v_fmac_f32_e32 v109, v104, v24
	v_fmac_f32_e32 v105, v104, v56
	v_mul_f32_e32 v104, v107, v55
	v_fmac_f32_e32 v104, v106, v54
	v_mul_f32_e32 v191, v107, v23
	v_add_f32_e32 v104, v105, v104
	v_fmac_f32_e32 v191, v106, v22
	v_add_f32_e32 v108, v108, v104
	ds_read_b128 v[104:107], v164
	v_add_f32_e32 v109, v109, v191
	v_add_f32_e32 v103, v103, v109
	s_waitcnt lgkmcnt(0)
	v_mul_f32_e32 v109, v105, v21
	v_mul_f32_e32 v105, v105, v53
	v_fmac_f32_e32 v109, v104, v20
	v_mul_f32_e32 v191, v107, v19
	v_fmac_f32_e32 v105, v104, v52
	v_mul_f32_e32 v104, v107, v51
	v_fmac_f32_e32 v191, v106, v18
	v_fmac_f32_e32 v104, v106, v50
	v_add_f32_e32 v109, v109, v191
	v_add_f32_e32 v104, v105, v104
	v_add_f32_e32 v103, v103, v109
	v_add_f32_e32 v104, v108, v104
	ds_read_b128 v[106:109], v165
	s_waitcnt lgkmcnt(0)
	v_mul_f32_e32 v105, v107, v49
	v_mul_f32_e32 v107, v107, v73
	v_fmac_f32_e32 v105, v106, v48
	v_fmac_f32_e32 v107, v106, v72
	v_mul_f32_e32 v106, v109, v71
	v_mul_f32_e32 v191, v109, v47
	v_fmac_f32_e32 v106, v108, v70
	v_fmac_f32_e32 v191, v108, v46
	v_add_f32_e32 v106, v107, v106
	v_add_f32_e32 v105, v105, v191
	v_add_f32_e32 v191, 0, v106
	ds_read_b128 v[106:109], v166
	v_add_f32_e32 v105, 0, v105
	s_waitcnt lgkmcnt(0)
	v_mul_f32_e32 v192, v107, v45
	v_mul_f32_e32 v107, v107, v81
	v_fmac_f32_e32 v192, v106, v44
	v_fmac_f32_e32 v107, v106, v80
	v_mul_f32_e32 v106, v109, v79
	v_fmac_f32_e32 v106, v108, v78
	v_mul_f32_e32 v193, v109, v43
	v_add_f32_e32 v106, v107, v106
	v_fmac_f32_e32 v193, v108, v42
	v_add_f32_e32 v191, v191, v106
	ds_read_b128 v[106:109], v167
	v_add_f32_e32 v192, v192, v193
	v_add_f32_e32 v105, v105, v192
	s_waitcnt lgkmcnt(0)
	v_mul_f32_e32 v192, v107, v41
	v_mul_f32_e32 v107, v107, v77
	v_fmac_f32_e32 v192, v106, v40
	v_fmac_f32_e32 v107, v106, v76
	v_mul_f32_e32 v106, v109, v75
	v_fmac_f32_e32 v106, v108, v74
	v_mul_f32_e32 v193, v109, v39
	v_add_f32_e32 v106, v107, v106
	v_fmac_f32_e32 v193, v108, v38
	v_add_f32_e32 v191, v191, v106
	ds_read_b128 v[106:109], v168
	v_add_f32_e32 v192, v192, v193
	v_add_f32_e32 v105, v105, v192
	s_waitcnt lgkmcnt(0)
	v_mul_f32_e32 v192, v107, v33
	v_mul_f32_e32 v107, v107, v65
	v_fmac_f32_e32 v192, v106, v32
	v_fmac_f32_e32 v107, v106, v64
	v_mul_f32_e32 v106, v109, v63
	v_fmac_f32_e32 v106, v108, v62
	v_mul_f32_e32 v193, v109, v31
	v_add_f32_e32 v106, v107, v106
	v_fmac_f32_e32 v193, v108, v30
	v_add_f32_e32 v191, v191, v106
	ds_read_b128 v[106:109], v169
	v_add_f32_e32 v192, v192, v193
	v_add_f32_e32 v105, v105, v192
	s_waitcnt lgkmcnt(0)
	v_mul_f32_e32 v192, v107, v37
	v_mul_f32_e32 v107, v107, v69
	v_fmac_f32_e32 v192, v106, v36
	v_fmac_f32_e32 v107, v106, v68
	v_mul_f32_e32 v106, v109, v67
	v_fmac_f32_e32 v106, v108, v66
	v_mul_f32_e32 v193, v109, v35
	v_add_f32_e32 v106, v107, v106
	v_fmac_f32_e32 v193, v108, v34
	v_add_f32_e32 v191, v191, v106
	ds_read_b128 v[106:109], v170
	v_add_f32_e32 v192, v192, v193
	v_add_f32_e32 v105, v105, v192
	s_waitcnt lgkmcnt(0)
	v_mul_f32_e32 v192, v107, v29
	v_mul_f32_e32 v107, v107, v61
	v_fmac_f32_e32 v192, v106, v28
	v_fmac_f32_e32 v107, v106, v60
	v_mul_f32_e32 v106, v109, v59
	v_fmac_f32_e32 v106, v108, v58
	v_mul_f32_e32 v193, v109, v27
	v_add_f32_e32 v106, v107, v106
	v_fmac_f32_e32 v193, v108, v26
	v_add_f32_e32 v191, v191, v106
	ds_read_b128 v[106:109], v171
	v_add_f32_e32 v192, v192, v193
	v_add_f32_e32 v105, v105, v192
	s_waitcnt lgkmcnt(0)
	v_mul_f32_e32 v192, v107, v25
	v_mul_f32_e32 v107, v107, v57
	v_fmac_f32_e32 v192, v106, v24
	v_fmac_f32_e32 v107, v106, v56
	v_mul_f32_e32 v106, v109, v55
	v_fmac_f32_e32 v106, v108, v54
	v_mul_f32_e32 v193, v109, v23
	v_add_f32_e32 v106, v107, v106
	v_fmac_f32_e32 v193, v108, v22
	v_add_f32_e32 v191, v191, v106
	ds_read_b128 v[106:109], v172
	v_add_f32_e32 v192, v192, v193
	v_add_f32_e32 v105, v105, v192
	s_waitcnt lgkmcnt(0)
	v_mul_f32_e32 v192, v107, v21
	v_mul_f32_e32 v193, v109, v19
	v_fmac_f32_e32 v192, v106, v20
	v_fmac_f32_e32 v193, v108, v18
	v_add_f32_e32 v192, v192, v193
	v_add_f32_e32 v105, v105, v192
	ds_read_b128 v[192:195], v173
	v_mul_f32_e32 v107, v107, v53
	v_fmac_f32_e32 v107, v106, v52
	v_mul_f32_e32 v106, v109, v51
	v_fmac_f32_e32 v106, v108, v50
	s_waitcnt lgkmcnt(0)
	v_mul_f32_e32 v49, v193, v49
	v_mul_f32_e32 v47, v195, v47
	v_fmac_f32_e32 v49, v192, v48
	v_fmac_f32_e32 v47, v194, v46
	v_add_f32_e32 v46, v49, v47
	v_add_f32_e32 v106, v107, v106
	v_add_f32_e32 v107, 0, v46
	v_mul_f32_e32 v46, v193, v73
	v_mul_f32_e32 v47, v195, v71
	v_fmac_f32_e32 v46, v192, v72
	v_fmac_f32_e32 v47, v194, v70
	v_add_f32_e32 v46, v46, v47
	v_add_f32_e32 v70, 0, v46
	ds_read_b128 v[46:49], v174
	v_add_f32_e32 v106, v191, v106
	s_waitcnt lgkmcnt(0)
	v_mul_f32_e32 v45, v47, v45
	v_mul_f32_e32 v43, v49, v43
	v_fmac_f32_e32 v45, v46, v44
	v_fmac_f32_e32 v43, v48, v42
	v_add_f32_e32 v42, v45, v43
	v_add_f32_e32 v71, v107, v42
	v_mul_f32_e32 v42, v47, v81
	v_mul_f32_e32 v43, v49, v79
	v_fmac_f32_e32 v42, v46, v80
	v_fmac_f32_e32 v43, v48, v78
	v_add_f32_e32 v42, v42, v43
	v_add_f32_e32 v46, v70, v42
	ds_read_b128 v[42:45], v175
	s_waitcnt lgkmcnt(0)
	v_mul_f32_e32 v41, v43, v41
	v_mul_f32_e32 v39, v45, v39
	v_fmac_f32_e32 v41, v42, v40
	v_fmac_f32_e32 v39, v44, v38
	v_add_f32_e32 v38, v41, v39
	v_add_f32_e32 v47, v71, v38
	v_mul_f32_e32 v38, v43, v77
	v_mul_f32_e32 v39, v45, v75
	v_fmac_f32_e32 v38, v42, v76
	v_fmac_f32_e32 v39, v44, v74
	v_add_f32_e32 v38, v38, v39
	v_add_f32_e32 v42, v46, v38
	ds_read_b128 v[38:41], v176
	s_waitcnt lgkmcnt(0)
	v_mul_f32_e32 v33, v39, v33
	v_mul_f32_e32 v31, v41, v31
	v_fmac_f32_e32 v33, v38, v32
	v_fmac_f32_e32 v31, v40, v30
	v_add_f32_e32 v30, v33, v31
	v_add_f32_e32 v43, v47, v30
	v_mul_f32_e32 v30, v39, v65
	v_mul_f32_e32 v31, v41, v63
	v_fmac_f32_e32 v30, v38, v64
	v_fmac_f32_e32 v31, v40, v62
	v_add_f32_e32 v30, v30, v31
	v_add_f32_e32 v38, v42, v30
	ds_read_b128 v[30:33], v177
	s_waitcnt lgkmcnt(0)
	v_mul_f32_e32 v37, v31, v37
	v_mul_f32_e32 v31, v31, v69
	v_fmac_f32_e32 v37, v30, v36
	v_fmac_f32_e32 v31, v30, v68
	v_mul_f32_e32 v30, v33, v67
	v_mul_f32_e32 v35, v33, v35
	v_fmac_f32_e32 v30, v32, v66
	v_fmac_f32_e32 v35, v32, v34
	v_add_f32_e32 v30, v31, v30
	v_add_f32_e32 v34, v37, v35
	v_add_f32_e32 v35, v38, v30
	ds_read_b128 v[30:33], v178
	v_add_f32_e32 v34, v43, v34
	s_waitcnt lgkmcnt(0)
	v_mul_f32_e32 v29, v31, v29
	v_mul_f32_e32 v27, v33, v27
	v_fmac_f32_e32 v29, v30, v28
	v_fmac_f32_e32 v27, v32, v26
	v_add_f32_e32 v26, v29, v27
	v_add_f32_e32 v34, v34, v26
	v_mul_f32_e32 v26, v31, v61
	v_mul_f32_e32 v27, v33, v59
	v_fmac_f32_e32 v26, v30, v60
	v_fmac_f32_e32 v27, v32, v58
	v_add_f32_e32 v26, v26, v27
	v_add_f32_e32 v30, v35, v26
	ds_read_b128 v[26:29], v179
	s_waitcnt lgkmcnt(0)
	v_mul_f32_e32 v25, v27, v25
	v_mul_f32_e32 v23, v29, v23
	v_fmac_f32_e32 v25, v26, v24
	v_fmac_f32_e32 v23, v28, v22
	v_add_f32_e32 v22, v25, v23
	v_add_f32_e32 v31, v34, v22
	v_mul_f32_e32 v22, v27, v57
	v_mul_f32_e32 v23, v29, v55
	v_fmac_f32_e32 v22, v26, v56
	v_fmac_f32_e32 v23, v28, v54
	v_add_f32_e32 v22, v22, v23
	v_add_f32_e32 v26, v30, v22
	ds_read_b128 v[22:25], v180
	v_cndmask_b32_e64 v27, v92, v104, s[34:35]
	v_cndmask_b32_e64 v28, v104, v92, s[34:35]
	v_cndmask_b32_e64 v29, v94, v106, s[34:35]
	v_cndmask_b32_e64 v30, v106, v94, s[34:35]
	s_waitcnt lgkmcnt(0)
	v_mul_f32_e32 v21, v23, v21
	v_mul_f32_e32 v19, v25, v19
	v_fmac_f32_e32 v21, v22, v20
	v_fmac_f32_e32 v19, v24, v18
	v_add_f32_e32 v18, v21, v19
	v_mul_f32_e32 v19, v23, v53
	v_mul_f32_e32 v20, v25, v51
	v_fmac_f32_e32 v19, v22, v52
	v_fmac_f32_e32 v20, v24, v50
	v_add_f32_e32 v19, v19, v20
	v_cndmask_b32_e64 v20, v2, v4, s[34:35]
	v_cndmask_b32_e64 v2, v4, v2, s[34:35]
	v_cndmask_b32_e64 v4, v82, v5, s[34:35]
	ds_bpermute_b32 v4, v112, v4
	v_cndmask_b32_e64 v5, v5, v82, s[34:35]
	ds_bpermute_b32 v20, v112, v20
	v_cndmask_b32_e64 v21, v86, v98, s[34:35]
	v_cndmask_b32_e64 v22, v98, v86, s[34:35]
	s_waitcnt lgkmcnt(1)
	v_add_f32_e32 v4, v5, v4
	v_cndmask_b32_e64 v5, v83, v6, s[34:35]
	ds_bpermute_b32 v5, v112, v5
	s_waitcnt lgkmcnt(1)
	v_add_f32_e32 v2, v2, v20
	v_cndmask_b32_e64 v6, v6, v83, s[34:35]
	v_cndmask_b32_e64 v20, v84, v7, s[34:35]
	v_cndmask_b32_e64 v7, v7, v84, s[34:35]
	s_waitcnt lgkmcnt(0)
	v_add_f32_e32 v5, v6, v5
	ds_bpermute_b32 v6, v112, v20
	v_cndmask_b32_e64 v20, v97, v85, s[34:35]
	v_cndmask_b32_e64 v23, v88, v100, s[34:35]
	v_cndmask_b32_e64 v24, v100, v88, s[34:35]
	v_cndmask_b32_e64 v25, v90, v102, s[34:35]
	s_waitcnt lgkmcnt(0)
	v_add_f32_e32 v6, v7, v6
	v_cndmask_b32_e64 v7, v85, v97, s[34:35]
	ds_bpermute_b32 v7, v112, v7
	v_add_f32_e32 v19, v26, v19
	v_cndmask_b32_e64 v26, v102, v90, s[34:35]
	v_add_f32_e32 v18, v31, v18
	s_waitcnt lgkmcnt(0)
	v_add_f32_e32 v7, v20, v7
	ds_bpermute_b32 v20, v112, v21
	v_cndmask_b32_e64 v21, v87, v99, s[34:35]
	ds_bpermute_b32 v21, v112, v21
	s_waitcnt lgkmcnt(1)
	v_add_f32_e32 v20, v22, v20
	v_cndmask_b32_e64 v22, v99, v87, s[34:35]
	s_waitcnt lgkmcnt(0)
	v_add_f32_e32 v21, v22, v21
	ds_bpermute_b32 v22, v112, v23
	v_cndmask_b32_e64 v23, v89, v101, s[34:35]
	ds_bpermute_b32 v23, v112, v23
	s_waitcnt lgkmcnt(1)
	v_add_f32_e32 v22, v24, v22
	v_cndmask_b32_e64 v24, v101, v89, s[34:35]
	s_waitcnt lgkmcnt(0)
	v_add_f32_e32 v23, v24, v23
	ds_bpermute_b32 v24, v112, v25
	v_cndmask_b32_e64 v25, v91, v103, s[34:35]
	ds_bpermute_b32 v25, v112, v25
	s_waitcnt lgkmcnt(1)
	v_add_f32_e32 v24, v26, v24
	v_cndmask_b32_e64 v26, v103, v91, s[34:35]
	s_waitcnt lgkmcnt(0)
	v_add_f32_e32 v25, v26, v25
	ds_bpermute_b32 v26, v112, v27
	v_cndmask_b32_e64 v27, v93, v105, s[34:35]
	ds_bpermute_b32 v27, v112, v27
	s_waitcnt lgkmcnt(1)
	v_add_f32_e32 v26, v28, v26
	v_cndmask_b32_e64 v28, v105, v93, s[34:35]
	s_waitcnt lgkmcnt(0)
	v_add_f32_e32 v27, v28, v27
	ds_bpermute_b32 v28, v112, v29
	v_cndmask_b32_e64 v29, v95, v18, s[34:35]
	ds_bpermute_b32 v29, v112, v29
	v_cndmask_b32_e64 v18, v18, v95, s[34:35]
	s_waitcnt lgkmcnt(1)
	v_add_f32_e32 v28, v30, v28
	v_cndmask_b32_e64 v30, v96, v19, s[34:35]
	s_waitcnt lgkmcnt(0)
	v_add_f32_e32 v18, v18, v29
	ds_bpermute_b32 v29, v112, v30
	v_cndmask_b32_e64 v19, v19, v96, s[34:35]
	s_waitcnt lgkmcnt(0)
	v_add_f32_e32 v19, v19, v29
	v_cndmask_b32_e64 v29, v2, v23, s[36:37]
	v_cndmask_b32_e64 v2, v23, v2, s[36:37]
	v_cndmask_b32_e64 v23, v4, v24, s[36:37]
	ds_bpermute_b32 v23, v111, v23
	v_cndmask_b32_e64 v4, v24, v4, s[36:37]
	ds_bpermute_b32 v24, v111, v29
	s_waitcnt lgkmcnt(1)
	v_add_f32_e32 v4, v4, v23
	v_cndmask_b32_e64 v23, v5, v25, s[36:37]
	ds_bpermute_b32 v23, v111, v23
	s_waitcnt lgkmcnt(1)
	v_add_f32_e32 v2, v2, v24
	v_cndmask_b32_e64 v5, v25, v5, s[36:37]
	v_cndmask_b32_e64 v24, v6, v26, s[36:37]
	v_cndmask_b32_e64 v6, v26, v6, s[36:37]
	s_waitcnt lgkmcnt(0)
	v_add_f32_e32 v5, v5, v23
	ds_bpermute_b32 v23, v111, v24
	v_cndmask_b32_e64 v24, v20, v28, s[36:37]
	v_cndmask_b32_e64 v20, v28, v20, s[36:37]
	s_waitcnt lgkmcnt(0)
	v_add_f32_e32 v6, v6, v23
	v_cndmask_b32_e64 v23, v7, v27, s[36:37]
	ds_bpermute_b32 v23, v111, v23
	v_cndmask_b32_e64 v7, v27, v7, s[36:37]
	s_waitcnt lgkmcnt(0)
	v_add_f32_e32 v7, v7, v23
	ds_bpermute_b32 v23, v111, v24
	s_waitcnt lgkmcnt(0)
	v_add_f32_e32 v20, v20, v23
	v_cndmask_b32_e64 v23, v21, v18, s[36:37]
	v_cndmask_b32_e64 v18, v18, v21, s[36:37]
	v_cndmask_b32_e64 v21, v22, v19, s[36:37]
	ds_bpermute_b32 v21, v111, v21
	v_cndmask_b32_e64 v19, v19, v22, s[36:37]
	ds_bpermute_b32 v22, v111, v23
	s_waitcnt lgkmcnt(1)
	v_add_f32_e32 v19, v19, v21
	v_cndmask_b32_e64 v21, v2, v7, s[38:39]
	v_cndmask_b32_e64 v2, v7, v2, s[38:39]
	v_cndmask_b32_e64 v7, v4, v20, s[38:39]
	ds_bpermute_b32 v7, v113, v7
	s_waitcnt lgkmcnt(1)
	v_add_f32_e32 v18, v18, v22
	v_cndmask_b32_e64 v4, v20, v4, s[38:39]
	ds_bpermute_b32 v20, v113, v21
	s_waitcnt lgkmcnt(1)
	v_add_f32_e32 v4, v4, v7
	v_cndmask_b32_e64 v7, v5, v18, s[38:39]
	ds_bpermute_b32 v7, v113, v7
	v_cndmask_b32_e64 v5, v18, v5, s[38:39]
	v_cndmask_b32_e64 v18, v6, v19, s[38:39]
	s_waitcnt lgkmcnt(1)
	v_add_f32_e32 v2, v2, v20
	v_cndmask_b32_e64 v6, v19, v6, s[38:39]
	s_waitcnt lgkmcnt(0)
	v_add_f32_e32 v5, v5, v7
	ds_bpermute_b32 v7, v113, v18
	s_waitcnt lgkmcnt(0)
	v_add_f32_e32 v6, v6, v7
	v_cndmask_b32_e64 v7, v2, v5, s[40:41]
	v_cndmask_b32_e64 v2, v5, v2, s[40:41]
	v_cndmask_b32_e64 v5, v4, v6, s[40:41]
	v_cndmask_b32_e64 v4, v6, v4, s[40:41]
	ds_bpermute_b32 v6, v114, v7
	ds_bpermute_b32 v5, v114, v5
	s_waitcnt lgkmcnt(1)
	v_add_f32_e32 v2, v2, v6
	s_waitcnt lgkmcnt(0)
	v_add_f32_e32 v4, v4, v5
	ds_bpermute_b32 v5, v115, v2
	s_waitcnt lgkmcnt(0)
	v_add_f32_e32 v2, v2, v5
	ds_bpermute_b32 v5, v115, v4
	s_waitcnt lgkmcnt(0)
	v_add_f32_e32 v4, v4, v5
	ds_bpermute_b32 v5, v116, v2
	s_waitcnt lgkmcnt(0)
	v_add_f32_e32 v2, v2, v5
	ds_bpermute_b32 v5, v116, v4
	s_waitcnt lgkmcnt(0)
	v_add_f32_e32 v5, v4, v5
	ds_bpermute_b32 v4, v114, v2
	ds_bpermute_b32 v6, v114, v5
	s_waitcnt lgkmcnt(1)
	v_max_f32_e32 v4, v4, v4
	v_max_f32_e32 v4, v2, v4
	ds_bpermute_b32 v7, v113, v4
	s_waitcnt lgkmcnt(1)
	v_max_f32_e32 v6, v6, v6
	v_max_f32_e32 v6, v5, v6
	s_waitcnt lgkmcnt(0)
	v_max_f32_e32 v7, v7, v7
	v_max_f32_e32 v4, v4, v7
	ds_bpermute_b32 v7, v113, v6
	s_waitcnt lgkmcnt(0)
	v_max_f32_e32 v7, v7, v7
	v_max_f32_e32 v6, v6, v7
	ds_bpermute_b32 v7, v111, v4
	s_waitcnt lgkmcnt(0)
	v_max_f32_e32 v7, v7, v7
	v_max_f32_e32 v4, v4, v7
	ds_bpermute_b32 v7, v111, v6
	s_waitcnt lgkmcnt(0)
	v_max_f32_e32 v7, v7, v7
	v_max_f32_e32 v6, v6, v7
	ds_bpermute_b32 v7, v112, v4
	s_waitcnt lgkmcnt(0)
	v_max_f32_e32 v7, v7, v7
	v_max_f32_e32 v4, v4, v7
	ds_bpermute_b32 v7, v112, v6
	v_sub_f32_e32 v2, v2, v4
	v_mul_f32_e32 v2, 0x3fb8aa3b, v2
	v_exp_f32_e32 v4, v2
	s_waitcnt lgkmcnt(0)
	v_max_f32_e32 v7, v7, v7
	v_max_f32_e32 v6, v6, v7
	v_sub_f32_e32 v2, v5, v6
	v_mul_f32_e32 v2, 0x3fb8aa3b, v2
	ds_bpermute_b32 v5, v114, v4
	v_exp_f32_e32 v2, v2
	s_waitcnt lgkmcnt(0)
	v_add_f32_e32 v5, v4, v5
	ds_bpermute_b32 v6, v114, v2
	ds_bpermute_b32 v7, v113, v5
	s_waitcnt lgkmcnt(1)
	v_add_f32_e32 v6, v2, v6
	s_waitcnt lgkmcnt(0)
	v_add_f32_e32 v5, v5, v7
	ds_bpermute_b32 v7, v113, v6
	s_waitcnt lgkmcnt(0)
	v_add_f32_e32 v6, v6, v7
	ds_bpermute_b32 v7, v111, v5
	s_waitcnt lgkmcnt(0)
	v_add_f32_e32 v7, v5, v7
	ds_bpermute_b32 v5, v111, v6
	ds_bpermute_b32 v18, v112, v7
	s_waitcnt lgkmcnt(1)
	v_add_f32_e32 v5, v6, v5
	ds_bpermute_b32 v6, v112, v5
	s_and_saveexec_b64 s[0:1], s[42:43]
	s_cbranch_execz .LBB0_2122
	s_waitcnt lgkmcnt(1)
	v_add_f32_e32 v7, v7, v18
	v_div_scale_f32 v18, s[2:3], v7, v7, v4
	v_rcp_f32_e32 v19, v18
	v_div_scale_f32 v20, vcc, v4, v7, v4
	s_cmp_eq_u32 s8, s48
	v_fma_f32 v21, -v18, v19, 1.0
	v_fmac_f32_e32 v19, v21, v19
	v_mul_f32_e32 v21, v20, v19
	v_fma_f32 v22, -v18, v21, v20
	v_fmac_f32_e32 v21, v22, v19
	v_fma_f32 v18, -v18, v21, v20
	v_div_fmas_f32 v18, v18, v19, v21
	v_div_fixup_f32 v4, v18, v7, v4
	v_lshl_add_u64 v[18:19], s[44:45], 0, v[14:15]
	global_store_dword v[18:19], v4, off
	s_cbranch_scc1 .LBB0_2122
	s_waitcnt lgkmcnt(0)
	v_add_f32_e32 v4, v5, v6
	v_div_scale_f32 v5, s[2:3], v4, v4, v2
	v_rcp_f32_e32 v6, v5
	v_div_scale_f32 v7, vcc, v2, v4, v2
	s_lshl_b64 s[2:3], s[48:49], 6
	v_fma_f32 v18, -v5, v6, 1.0
	v_fmac_f32_e32 v6, v18, v6
	v_mul_f32_e32 v18, v7, v6
	v_fma_f32 v19, -v5, v18, v7
	v_fmac_f32_e32 v18, v19, v6
	v_fma_f32 v5, -v5, v18, v7
	v_div_fmas_f32 v5, v5, v6, v18
	v_div_fixup_f32 v2, v5, v4, v2
	v_lshl_add_u64 v[4:5], v[10:11], 0, s[2:3]
	global_store_dword v[4:5], v2, off
	s_branch .LBB0_2122
